# v68 + conv tap loop: the zero initialisation of a row's weights only on the path that skips their load
# speedup vs baseline: 1.0283x; 1.0021x over previous
; #define LAS __attribute__((address_space(3)))
; __device__ __forceinline__ void ph_convpool_fast(const Args& a, LAS unsigned char* lds) {
;     ...
;         for (int r0 = 0; r0 < 36; r0 += 4) {
; #pragma unroll
;             for (int u = 0; u < 4; ++u) { const int r = r0 + u;
;                 if (r < 31) unpack8(*(const LAS u32x4*)(lds + CW_OFF + r * 1024 + ch * 2), wq[u]);
;                 else {
; #pragma unroll
;                     for (int c = 0; c < 8; ++c) wq[u][c] = 0.f; }
;                 float v[8]; unpack8(*(const LAS u32x4*)(lds + VT_OFF + (4 * wave + (r < 33 ? r : 33)) * 1024 + ch * 2), v);
; #pragma unroll
;                 for (int j = 0; j < 4; ++j)
; #pragma unroll
;                     for (int c = 0; c < 8; ++c) acc[j][c] += wq[(u - j) & 3][c] * v[c];
;             }
.LBB0_295:
	s_add_i32 s3, s2, -3
	s_cmp_lt_u32 s3, 31
	s_cbranch_scc0 .Lconv_zero_w0
	ds_read_b128 v[26:29], v181
	s_waitcnt lgkmcnt(0)
	v_lshlrev_b32_e32 v122, 16, v26
	v_lshlrev_b32_e32 v123, 16, v27
	v_and_b32_e32 v119, 0xffff0000, v27
	v_and_b32_e32 v118, 0xffff0000, v26
	v_lshlrev_b32_e32 v116, 16, v28
	v_lshlrev_b32_e32 v117, 16, v29
	v_and_b32_e32 v111, 0xffff0000, v29
	v_and_b32_e32 v110, 0xffff0000, v28
.LBB0_297:
	v_add_u32_e32 v30, v181, v140
	v_add_u32_e32 v26, 0xfffe4c00, v30
	ds_read_b128 v[26:29], v26
	s_add_i32 s8, s3, 1
	s_cmp_gt_u32 s8, 30
	s_cbranch_scc1 .Lconv_zero_w1
	ds_read_b128 v[32:35], v181 offset:1024
	s_waitcnt lgkmcnt(0)
	v_lshlrev_b32_e32 v100, 16, v32
	v_lshlrev_b32_e32 v101, 16, v33
	v_and_b32_e32 v105, 0xffff0000, v33
	v_and_b32_e32 v104, 0xffff0000, v32
	v_lshlrev_b32_e32 v108, 16, v34
	v_lshlrev_b32_e32 v109, 16, v35
	v_and_b32_e32 v115, 0xffff0000, v35
	v_and_b32_e32 v114, 0xffff0000, v34
.LBB0_299:
	v_add_u32_e32 v30, 0xfffe5000, v30
	ds_read_b128 v[30:33], v30
	s_add_i32 s8, s8, 1
	s_cmp_gt_u32 s8, 30
	s_cbranch_scc1 .Lconv_zero_w2
	ds_read_b128 v[34:37], v181 offset:2048
	s_waitcnt lgkmcnt(0)
	v_lshlrev_b32_e32 v124, 16, v34
	v_lshlrev_b32_e32 v125, 16, v35
	v_and_b32_e32 v127, 0xffff0000, v35
	v_and_b32_e32 v126, 0xffff0000, v34
	v_lshlrev_b32_e32 v128, 16, v36
	v_lshlrev_b32_e32 v129, 16, v37
	v_and_b32_e32 v113, 0xffff0000, v37
	v_and_b32_e32 v112, 0xffff0000, v36
.LBB0_301:
	s_add_i32 s8, s2, -1
	s_min_u32 s8, s8, 33
	v_lshl_add_u32 v34, s8, 10, v151
	ds_read_b128 v[34:37], v34
	s_cmp_gt_u32 s2, 30
	s_cbranch_scc1 .Lconv_zero_w3
	ds_read_b128 v[134:137], v181 offset:3072
	s_waitcnt lgkmcnt(0)
	v_lshlrev_b32_e32 v130, 16, v134
	v_lshlrev_b32_e32 v131, 16, v135
	v_and_b32_e32 v133, 0xffff0000, v135
	v_and_b32_e32 v132, 0xffff0000, v134
	v_lshlrev_b32_e32 v134, 16, v136
	v_lshlrev_b32_e32 v135, 16, v137
	v_and_b32_e32 v137, 0xffff0000, v137
	v_and_b32_e32 v136, 0xffff0000, v136
	s_branch .LBB0_294
.Lconv_zero_w0:
	v_mov_b32_e32 v110, 0
	v_mov_b32_e32 v111, 0
	v_mov_b32_e32 v116, 0
	v_mov_b32_e32 v117, 0
	v_mov_b32_e32 v118, 0
	v_mov_b32_e32 v119, 0
	v_mov_b32_e32 v122, 0
	v_mov_b32_e32 v123, 0
	s_branch .LBB0_297
.Lconv_zero_w1:
	v_mov_b32_e32 v114, 0
	v_mov_b32_e32 v115, 0
	v_mov_b32_e32 v108, 0
	v_mov_b32_e32 v109, 0
	v_mov_b32_e32 v104, 0
	v_mov_b32_e32 v105, 0
	v_mov_b32_e32 v100, 0
	v_mov_b32_e32 v101, 0
	s_branch .LBB0_299
.Lconv_zero_w2:
	v_mov_b32_e32 v112, 0
	v_mov_b32_e32 v113, 0
	v_mov_b32_e32 v128, 0
	v_mov_b32_e32 v129, 0
	v_mov_b32_e32 v126, 0
	v_mov_b32_e32 v127, 0
	v_mov_b32_e32 v124, 0
	v_mov_b32_e32 v125, 0
	s_branch .LBB0_301
.Lconv_zero_w3:
	v_mov_b32_e32 v136, 0
	v_mov_b32_e32 v137, 0
	v_mov_b32_e32 v134, 0
	v_mov_b32_e32 v135, 0
	v_mov_b32_e32 v132, 0
	v_mov_b32_e32 v133, 0
	v_mov_b32_e32 v130, 0
	v_mov_b32_e32 v131, 0
	s_branch .LBB0_294

; __device__ __forceinline__ u32x4 pack8(const f32x4 v0, const f32x4 v1) { u32x4 w; w.x = cvt_pk_bf16(v0[0], v0[1]); w.y = cvt_pk_bf16(v0[2], v0[3]); w.z = cvt_pk_bf16(v1[0], v1[1]); w.w = cvt_pk_bf16(v1[2], v1[3]); return w; }
; #define EPI_ROWLOOP for (int ai = 0; ai < 2; ++ai) _Pragma("unroll") for (int m = 0; m < 4; ++m)
; __device__ __forceinline__ float gelu_tanh(float x) {
;     const float u = 0.7978845608028654f * (x + 0.044715f * x * x * x);
;     const float e = __expf(2.0f * u);
;     const float th = 1.0f - 2.0f / (e + 1.0f);
;     return 0.5f * x * (1.0f + th);
; }
;     __device__ __forceinline__ void operator()(const f32x4 (&acc)[2][2][4][2], const pg8::Unit& u, int wr, int wc, int fr, int fq) const {
;         const int row0 = u.pm * 256 + wr * 64 + fr, cl = wc * 32 + 8 * fq;
;         const f32x4 b0 = *(const f32x4*)(bias1 + u.pn * 128 + cl), b1 = *(const f32x4*)(bias1 + u.pn * 128 + cl + 4);
; #pragma unroll
;         EPI_ROWLOOP { f32x4 v0 = acc[ai][0][m][0] * (1.0f / (X8_SCALE * W8_SCALE)) + b0, v1 = acc[ai][0][m][1] * (1.0f / (X8_SCALE * W8_SCALE)) + b1;
; #pragma unroll
;             for (int i = 0; i < 4; ++i) { v0[i] = gelu_tanh(v0[i]); v1[i] = gelu_tanh(v1[i]); }
;             *(u32x4*)(CH1 + ((size_t)u.pn * 8192 + row0 + ai * 128 + m * 16) * 128 + cl) = pack8(v0, v1); }
;     }
.LBB0_1432:
	s_lshl_b32 s12, s52, 7
	v_lshl_add_u64 v[2:3], s[12:13], 2, v[84:85]
	global_load_dwordx4 v[6:9], v[2:3], off
	s_nop 0
	global_load_dwordx4 v[2:5], v[2:3], off offset:16
	v_lshl_add_u32 v10, s53, 8, v91
	v_ashrrev_i32_e32 v11, 31, v10
	s_lshl_b32 s12, s52, 21
	v_lshlrev_b64 v[10:11], 8, v[10:11]
	s_waitcnt vmcnt(0)
	v_pk_fma_f32 v[16:17], v[78:79], s[20:21], v[6:7] op_sel_hi:[1,0,1]
	v_pk_fma_f32 v[14:15], v[80:81], s[20:21], v[8:9] op_sel_hi:[1,0,1]
	v_mul_f32_e32 v80, 0x3d372713, v16
	v_mul_f32_e32 v95, 0x3d372713, v17
	v_mul_f32_e32 v80, v16, v80
	v_mul_f32_e32 v95, v17, v95
	v_pk_fma_f32 v[12:13], v[76:77], s[20:21], v[4:5] op_sel_hi:[1,0,1]
	v_pk_mul_f32 v[76:77], v[16:17], 0.5 op_sel_hi:[1,0]
	v_fma_f32 v16, v16, v80, v16
	v_fma_f32 v17, v17, v95, v17
	v_mul_f32_e32 v16, 0x3f4c422a, v16
	v_mul_f32_e32 v17, 0x3f4c422a, v17
	v_add_f32_e32 v16, v16, v16
	v_add_f32_e32 v17, v17, v17
	v_mul_f32_e32 v16, 0x3fb8aa3b, v16
	v_mul_f32_e32 v17, 0x3fb8aa3b, v17
	v_exp_f32_e32 v16, v16
	v_exp_f32_e32 v17, v17
	v_pk_fma_f32 v[74:75], v[74:75], s[20:21], v[2:3] op_sel_hi:[1,0,1]
	v_mul_f32_e32 v97, 0x3d372713, v14
	v_mul_f32_e32 v81, 0x3d372713, v74
	v_mul_f32_e32 v96, 0x3d372713, v75
	v_mul_f32_e32 v81, v74, v81
	v_mul_f32_e32 v96, v75, v96
	v_pk_mul_f32 v[78:79], v[74:75], 0.5 op_sel_hi:[1,0]
	v_fma_f32 v74, v74, v81, v74
	v_fma_f32 v75, v75, v96, v75
	v_pk_add_f32 v[16:17], v[16:17], 1.0 op_sel_hi:[1,0]
	v_mul_f32_e32 v74, 0x3f4c422a, v74
	v_mul_f32_e32 v75, 0x3f4c422a, v75
	v_add_f32_e32 v74, v74, v74
	v_add_f32_e32 v75, v75, v75
	v_mul_f32_e32 v74, 0x3fb8aa3b, v74
	v_mul_f32_e32 v75, 0x3fb8aa3b, v75
	v_exp_f32_e32 v74, v74
	v_exp_f32_e32 v75, v75
	v_mul_f32_e32 v97, v14, v97
	v_fma_f32 v80, v14, v97, v14
	v_pk_add_f32 v[74:75], v[74:75], 1.0 op_sel_hi:[1,0]
	v_rcp_f32_e32 v17, v17
	s_nop 0
	v_add_f32_e32 v17, v17, v17
	v_rcp_f32_e32 v16, v16
	s_nop 0
	v_add_f32_e32 v16, v16, v16
	v_pk_add_f32 v[16:17], v[16:17], 1.0 op_sel_hi:[1,0] neg_lo:[1,0] neg_hi:[1,0]
	v_mul_f32_e32 v99, 0x3d372713, v15
	v_pk_add_f32 v[16:17], v[16:17], 1.0 op_sel_hi:[1,0]
	v_pk_mul_f32 v[16:17], v[76:77], v[16:17]
	v_mul_f32_e32 v76, v15, v99
	v_fma_f32 v76, v15, v76, v15
	v_mul_f32_e32 v80, 0x3f4c422a, v80
	v_mul_f32_e32 v76, 0x3f4c422a, v76
	v_add_f32_e32 v80, v80, v80
	v_add_f32_e32 v76, v76, v76
	v_mul_f32_e32 v80, 0x3fb8aa3b, v80
	v_rcp_f32_e32 v75, v75
	s_nop 0
	v_add_f32_e32 v75, v75, v75
	v_mul_f32_e32 v76, 0x3fb8aa3b, v76
	v_exp_f32_e32 v80, v80
	v_rcp_f32_e32 v74, v74
	s_nop 0
	v_add_f32_e32 v74, v74, v74
	v_exp_f32_e32 v81, v76
	v_mul_f32_e32 v98, 0x3d372713, v12
	v_pk_add_f32 v[74:75], v[74:75], 1.0 op_sel_hi:[1,0] neg_lo:[1,0] neg_hi:[1,0]
	v_mul_f32_e32 v76, v12, v98
	v_pk_add_f32 v[74:75], v[74:75], 1.0 op_sel_hi:[1,0]
	v_fma_f32 v76, v12, v76, v12
	v_pk_mul_f32 v[74:75], v[78:79], v[74:75]
	v_mul_f32_e32 v78, 0x3f4c422a, v76
	v_pk_add_f32 v[76:77], v[80:81], 1.0 op_sel_hi:[1,0]
	v_add_f32_e32 v78, v78, v78
	v_mul_f32_e32 v78, 0x3fb8aa3b, v78
	v_exp_f32_e32 v78, v78
	v_pk_mul_f32 v[14:15], v[14:15], 0.5 op_sel_hi:[1,0]
	v_rcp_f32_e32 v77, v77
	s_nop 0
	v_add_f32_e32 v77, v77, v77
	v_pk_fma_f32 v[66:67], v[66:67], s[20:21], v[2:3] op_sel_hi:[1,0,1]
	v_mul_f32_e32 v79, 0x3d372713, v13
	v_mul_f32_e32 v79, v13, v79
	v_fma_f32 v79, v13, v79, v13
	v_mul_f32_e32 v79, 0x3f4c422a, v79
	v_add_f32_e32 v79, v79, v79
	v_mul_f32_e32 v79, 0x3fb8aa3b, v79
	v_exp_f32_e32 v79, v79
	v_rcp_f32_e32 v76, v76
	s_nop 0
	v_add_f32_e32 v76, v76, v76
	v_pk_add_f32 v[76:77], v[76:77], 1.0 op_sel_hi:[1,0] neg_lo:[1,0] neg_hi:[1,0]
	v_pk_add_f32 v[78:79], v[78:79], 1.0 op_sel_hi:[1,0]
	v_pk_add_f32 v[76:77], v[76:77], 1.0 op_sel_hi:[1,0]
	v_pk_mul_f32 v[76:77], v[14:15], v[76:77]
	v_pk_mul_f32 v[12:13], v[12:13], 0.5 op_sel_hi:[1,0]
	v_pk_fma_f32 v[68:69], v[68:69], s[20:21], v[4:5] op_sel_hi:[1,0,1]
	v_rcp_f32_e32 v15, v79
	s_nop 0
	v_add_f32_e32 v15, v15, v15
	v_pk_fma_f32 v[58:59], v[58:59], s[20:21], v[2:3] op_sel_hi:[1,0,1]
	v_rcp_f32_e32 v14, v78
	s_nop 0
	v_add_f32_e32 v14, v14, v14
	v_pk_add_f32 v[14:15], v[14:15], 1.0 op_sel_hi:[1,0] neg_lo:[1,0] neg_hi:[1,0]
	v_pk_fma_f32 v[60:61], v[60:61], s[20:21], v[4:5] op_sel_hi:[1,0,1]
	v_pk_add_f32 v[14:15], v[14:15], 1.0 op_sel_hi:[1,0]
	v_pk_fma_f32 v[50:51], v[50:51], s[20:21], v[2:3] op_sel_hi:[1,0,1]
	v_pk_mul_f32 v[12:13], v[12:13], v[14:15]
	v_cvt_pk_bf16_f32 v14, v16, v17
	v_cvt_pk_bf16_f32 v17, v12, v13
	v_lshl_add_u64 v[12:13], v[10:11], 0, s[12:13]
	v_lshl_add_u64 v[10:11], s[16:17], 0, v[12:13]
	v_cvt_pk_bf16_f32 v15, v76, v77
	v_cvt_pk_bf16_f32 v16, v74, v75
	v_lshl_add_u64 v[10:11], v[10:11], 0, v[82:83]
	global_store_dwordx4 v[10:11], v[14:17], off
	v_pk_fma_f32 v[52:53], v[52:53], s[20:21], v[4:5] op_sel_hi:[1,0,1]
	v_pk_fma_f32 v[42:43], v[42:43], s[20:21], v[2:3] op_sel_hi:[1,0,1]
	v_pk_fma_f32 v[16:17], v[70:71], s[20:21], v[6:7] op_sel_hi:[1,0,1]
	v_pk_fma_f32 v[14:15], v[72:73], s[20:21], v[8:9] op_sel_hi:[1,0,1]
	v_mul_f32_e32 v70, 0x3d372713, v16
	v_mul_f32_e32 v71, 0x3d372713, v17
	v_mul_f32_e32 v70, v16, v70
	v_mul_f32_e32 v71, v17, v71
	v_fma_f32 v70, v16, v70, v16
	v_fma_f32 v71, v17, v71, v17
	v_mul_f32_e32 v70, 0x3f4c422a, v70
	v_mul_f32_e32 v71, 0x3f4c422a, v71
	v_add_f32_e32 v70, v70, v70
	v_add_f32_e32 v71, v71, v71
	v_mul_f32_e32 v70, 0x3fb8aa3b, v70
	v_mul_f32_e32 v71, 0x3fb8aa3b, v71
	v_exp_f32_e32 v70, v70
	v_exp_f32_e32 v71, v71
	v_mul_f32_e32 v72, 0x3d372713, v66
	v_mul_f32_e32 v72, v66, v72
	v_fma_f32 v72, v66, v72, v66
	v_pk_add_f32 v[70:71], v[70:71], 1.0 op_sel_hi:[1,0]
	v_mul_f32_e32 v72, 0x3f4c422a, v72
	v_add_f32_e32 v72, v72, v72
	v_mul_f32_e32 v72, 0x3fb8aa3b, v72
; __device__ __forceinline__ u32x4 pack8(const f32x4 v0, const f32x4 v1) { u32x4 w; w.x = cvt_pk_bf16(v0[0], v0[1]); w.y = cvt_pk_bf16(v0[2], v0[3]); w.z = cvt_pk_bf16(v1[0], v1[1]); w.w = cvt_pk_bf16(v1[2], v1[3]); return w; }
; #define EPI_ROWLOOP for (int ai = 0; ai < 2; ++ai) _Pragma("unroll") for (int m = 0; m < 4; ++m)
; __device__ __forceinline__ float gelu_tanh(float x) {
;     const float u = 0.7978845608028654f * (x + 0.044715f * x * x * x);
;     const float e = __expf(2.0f * u);
;     const float th = 1.0f - 2.0f / (e + 1.0f);
;     return 0.5f * x * (1.0f + th);
; }
;     __device__ __forceinline__ void operator()(const f32x4 (&acc)[2][2][4][2], const pg8::Unit& u, int wr, int wc, int fr, int fq) const {
;         const int row0 = u.pm * 256 + wr * 64 + fr, cl = wc * 32 + 8 * fq;
;         const f32x4 b0 = *(const f32x4*)(bias1 + u.pn * 128 + cl), b1 = *(const f32x4*)(bias1 + u.pn * 128 + cl + 4);
; #pragma unroll
;         EPI_ROWLOOP { f32x4 v0 = acc[ai][0][m][0] * (1.0f / (X8_SCALE * W8_SCALE)) + b0, v1 = acc[ai][0][m][1] * (1.0f / (X8_SCALE * W8_SCALE)) + b1;
; #pragma unroll
;             for (int i = 0; i < 4; ++i) { v0[i] = gelu_tanh(v0[i]); v1[i] = gelu_tanh(v1[i]); }
;             *(u32x4*)(CH1 + ((size_t)u.pn * 8192 + row0 + ai * 128 + m * 16) * 128 + cl) = pack8(v0, v1); }
;     }
	v_exp_f32_e32 v72, v72
	v_rcp_f32_e32 v71, v71
	s_nop 0
	v_add_f32_e32 v71, v71, v71
	v_pk_mul_f32 v[16:17], v[16:17], 0.5 op_sel_hi:[1,0]
	v_mul_f32_e32 v73, 0x3d372713, v67
	v_mul_f32_e32 v73, v67, v73
	v_fma_f32 v73, v67, v73, v67
	v_mul_f32_e32 v73, 0x3f4c422a, v73
	v_add_f32_e32 v73, v73, v73
	v_mul_f32_e32 v73, 0x3fb8aa3b, v73
	v_exp_f32_e32 v73, v73
	v_rcp_f32_e32 v70, v70
	s_nop 0
	v_add_f32_e32 v70, v70, v70
	v_pk_add_f32 v[70:71], v[70:71], 1.0 op_sel_hi:[1,0] neg_lo:[1,0] neg_hi:[1,0]
	v_pk_add_f32 v[72:73], v[72:73], 1.0 op_sel_hi:[1,0]
	v_pk_add_f32 v[70:71], v[70:71], 1.0 op_sel_hi:[1,0]
	v_pk_mul_f32 v[16:17], v[16:17], v[70:71]
	v_pk_mul_f32 v[66:67], v[66:67], 0.5 op_sel_hi:[1,0]
	v_pk_fma_f32 v[34:35], v[34:35], s[20:21], v[2:3] op_sel_hi:[1,0,1]
	v_rcp_f32_e32 v71, v73
	s_nop 0
	v_add_f32_e32 v71, v71, v71
	v_pk_fma_f32 v[36:37], v[36:37], s[20:21], v[4:5] op_sel_hi:[1,0,1]
	v_rcp_f32_e32 v70, v72
	s_nop 0
	v_add_f32_e32 v70, v70, v70
	v_pk_add_f32 v[70:71], v[70:71], 1.0 op_sel_hi:[1,0] neg_lo:[1,0] neg_hi:[1,0]
	v_mul_f32_e32 v72, 0x3d372713, v68
	v_pk_add_f32 v[70:71], v[70:71], 1.0 op_sel_hi:[1,0]
	v_mul_f32_e32 v72, v68, v72
	v_pk_mul_f32 v[66:67], v[66:67], v[70:71]
	v_mul_f32_e32 v70, 0x3d372713, v14
	v_mul_f32_e32 v71, 0x3d372713, v15
	v_mul_f32_e32 v70, v14, v70
	v_mul_f32_e32 v71, v15, v71
	v_fma_f32 v70, v14, v70, v14
	v_fma_f32 v71, v15, v71, v15
	v_mul_f32_e32 v70, 0x3f4c422a, v70
	v_mul_f32_e32 v71, 0x3f4c422a, v71
	v_add_f32_e32 v70, v70, v70
	v_add_f32_e32 v71, v71, v71
	v_mul_f32_e32 v70, 0x3fb8aa3b, v70
	v_mul_f32_e32 v71, 0x3fb8aa3b, v71
	v_exp_f32_e32 v70, v70
	v_exp_f32_e32 v71, v71
	v_fma_f32 v72, v68, v72, v68
	v_mul_f32_e32 v72, 0x3f4c422a, v72
	v_add_f32_e32 v72, v72, v72
	v_pk_add_f32 v[70:71], v[70:71], 1.0 op_sel_hi:[1,0]
	v_mul_f32_e32 v72, 0x3fb8aa3b, v72
	v_exp_f32_e32 v72, v72
	v_pk_mul_f32 v[14:15], v[14:15], 0.5 op_sel_hi:[1,0]
	v_pk_fma_f32 v[26:27], v[26:27], s[20:21], v[2:3] op_sel_hi:[1,0,1]
	v_rcp_f32_e32 v71, v71
	s_nop 0
	v_add_f32_e32 v71, v71, v71
	v_pk_fma_f32 v[2:3], v[18:19], s[20:21], v[2:3] op_sel_hi:[1,0,1]
	v_mul_f32_e32 v73, 0x3d372713, v69
	v_mul_f32_e32 v73, v69, v73
	v_fma_f32 v73, v69, v73, v69
	v_mul_f32_e32 v73, 0x3f4c422a, v73
	v_add_f32_e32 v73, v73, v73
	v_mul_f32_e32 v73, 0x3fb8aa3b, v73
	v_exp_f32_e32 v73, v73
	v_rcp_f32_e32 v70, v70
	s_nop 0
	v_add_f32_e32 v70, v70, v70
	v_pk_add_f32 v[70:71], v[70:71], 1.0 op_sel_hi:[1,0] neg_lo:[1,0] neg_hi:[1,0]
	v_pk_add_f32 v[72:73], v[72:73], 1.0 op_sel_hi:[1,0]
	v_pk_add_f32 v[70:71], v[70:71], 1.0 op_sel_hi:[1,0]
	v_pk_mul_f32 v[70:71], v[14:15], v[70:71]
	v_pk_mul_f32 v[68:69], v[68:69], 0.5 op_sel_hi:[1,0]
	v_rcp_f32_e32 v15, v73
	s_nop 0
	v_add_f32_e32 v15, v15, v15
	v_rcp_f32_e32 v14, v72
	s_nop 0
	v_add_f32_e32 v14, v14, v14
	v_pk_add_f32 v[14:15], v[14:15], 1.0 op_sel_hi:[1,0] neg_lo:[1,0] neg_hi:[1,0]
	s_nop 0
	v_pk_add_f32 v[14:15], v[14:15], 1.0 op_sel_hi:[1,0]
	s_nop 0
	v_pk_mul_f32 v[68:69], v[68:69], v[14:15]
	v_cvt_pk_bf16_f32 v14, v16, v17
	v_cvt_pk_bf16_f32 v16, v66, v67
	v_or_b32_e32 v66, 0x1000, v12
	v_mov_b32_e32 v67, v13
	v_cvt_pk_bf16_f32 v15, v70, v71
	v_cvt_pk_bf16_f32 v17, v68, v69
	v_lshl_add_u64 v[66:67], v[86:87], 0, v[66:67]
	global_store_dwordx4 v[66:67], v[14:17], off
	s_nop 1
	v_pk_fma_f32 v[16:17], v[62:63], s[20:21], v[6:7] op_sel_hi:[1,0,1]
	v_pk_fma_f32 v[14:15], v[64:65], s[20:21], v[8:9] op_sel_hi:[1,0,1]
	v_mul_f32_e32 v62, 0x3d372713, v16
	v_mul_f32_e32 v63, 0x3d372713, v17
	v_mul_f32_e32 v62, v16, v62
	v_mul_f32_e32 v63, v17, v63
	v_fma_f32 v62, v16, v62, v16
	v_fma_f32 v63, v17, v63, v17
	v_mul_f32_e32 v62, 0x3f4c422a, v62
	v_mul_f32_e32 v63, 0x3f4c422a, v63
	v_add_f32_e32 v62, v62, v62
	v_add_f32_e32 v63, v63, v63
	v_mul_f32_e32 v62, 0x3fb8aa3b, v62
	v_mul_f32_e32 v63, 0x3fb8aa3b, v63
	v_exp_f32_e32 v62, v62
	v_exp_f32_e32 v63, v63
	v_mul_f32_e32 v64, 0x3d372713, v58
	v_mul_f32_e32 v64, v58, v64
	v_fma_f32 v64, v58, v64, v58
	v_pk_add_f32 v[62:63], v[62:63], 1.0 op_sel_hi:[1,0]
	v_mul_f32_e32 v64, 0x3f4c422a, v64
	v_add_f32_e32 v64, v64, v64
	v_mul_f32_e32 v64, 0x3fb8aa3b, v64
	v_exp_f32_e32 v64, v64
	v_rcp_f32_e32 v63, v63
	s_nop 0
	v_add_f32_e32 v63, v63, v63
	v_pk_mul_f32 v[16:17], v[16:17], 0.5 op_sel_hi:[1,0]
	v_mul_f32_e32 v65, 0x3d372713, v59
	v_mul_f32_e32 v65, v59, v65
	v_fma_f32 v65, v59, v65, v59
	v_mul_f32_e32 v65, 0x3f4c422a, v65
	v_add_f32_e32 v65, v65, v65
	v_mul_f32_e32 v65, 0x3fb8aa3b, v65
	v_exp_f32_e32 v65, v65
	v_rcp_f32_e32 v62, v62
	s_nop 0
	v_add_f32_e32 v62, v62, v62
	v_pk_add_f32 v[62:63], v[62:63], 1.0 op_sel_hi:[1,0] neg_lo:[1,0] neg_hi:[1,0]
	v_pk_add_f32 v[64:65], v[64:65], 1.0 op_sel_hi:[1,0]
	v_pk_add_f32 v[62:63], v[62:63], 1.0 op_sel_hi:[1,0]
	v_pk_mul_f32 v[16:17], v[16:17], v[62:63]
	v_pk_mul_f32 v[58:59], v[58:59], 0.5 op_sel_hi:[1,0]
	v_rcp_f32_e32 v63, v65
	s_nop 0
	v_add_f32_e32 v63, v63, v63
	v_rcp_f32_e32 v62, v64
	s_nop 0
	v_add_f32_e32 v62, v62, v62
	v_pk_add_f32 v[62:63], v[62:63], 1.0 op_sel_hi:[1,0] neg_lo:[1,0] neg_hi:[1,0]
	v_mul_f32_e32 v64, 0x3d372713, v60
	v_pk_add_f32 v[62:63], v[62:63], 1.0 op_sel_hi:[1,0]
	v_mul_f32_e32 v64, v60, v64
	v_pk_mul_f32 v[58:59], v[58:59], v[62:63]
	v_mul_f32_e32 v62, 0x3d372713, v14
	v_mul_f32_e32 v63, 0x3d372713, v15
	v_mul_f32_e32 v62, v14, v62
	v_mul_f32_e32 v63, v15, v63
	v_fma_f32 v62, v14, v62, v14
	v_fma_f32 v63, v15, v63, v15
	v_mul_f32_e32 v62, 0x3f4c422a, v62
	v_mul_f32_e32 v63, 0x3f4c422a, v63
	v_add_f32_e32 v62, v62, v62
	v_add_f32_e32 v63, v63, v63
	v_mul_f32_e32 v62, 0x3fb8aa3b, v62
	v_mul_f32_e32 v63, 0x3fb8aa3b, v63
	v_exp_f32_e32 v62, v62
	v_exp_f32_e32 v63, v63
; __device__ __forceinline__ u32x4 pack8(const f32x4 v0, const f32x4 v1) { u32x4 w; w.x = cvt_pk_bf16(v0[0], v0[1]); w.y = cvt_pk_bf16(v0[2], v0[3]); w.z = cvt_pk_bf16(v1[0], v1[1]); w.w = cvt_pk_bf16(v1[2], v1[3]); return w; }
; #define EPI_ROWLOOP for (int ai = 0; ai < 2; ++ai) _Pragma("unroll") for (int m = 0; m < 4; ++m)
; __device__ __forceinline__ float gelu_tanh(float x) {
;     const float u = 0.7978845608028654f * (x + 0.044715f * x * x * x);
;     const float e = __expf(2.0f * u);
;     const float th = 1.0f - 2.0f / (e + 1.0f);
;     return 0.5f * x * (1.0f + th);
; }
;     __device__ __forceinline__ void operator()(const f32x4 (&acc)[2][2][4][2], const pg8::Unit& u, int wr, int wc, int fr, int fq) const {
;         const int row0 = u.pm * 256 + wr * 64 + fr, cl = wc * 32 + 8 * fq;
;         const f32x4 b0 = *(const f32x4*)(bias1 + u.pn * 128 + cl), b1 = *(const f32x4*)(bias1 + u.pn * 128 + cl + 4);
; #pragma unroll
;         EPI_ROWLOOP { f32x4 v0 = acc[ai][0][m][0] * (1.0f / (X8_SCALE * W8_SCALE)) + b0, v1 = acc[ai][0][m][1] * (1.0f / (X8_SCALE * W8_SCALE)) + b1;
; #pragma unroll
;             for (int i = 0; i < 4; ++i) { v0[i] = gelu_tanh(v0[i]); v1[i] = gelu_tanh(v1[i]); }
;             *(u32x4*)(CH1 + ((size_t)u.pn * 8192 + row0 + ai * 128 + m * 16) * 128 + cl) = pack8(v0, v1); }
;     }
	v_fma_f32 v64, v60, v64, v60
	v_mul_f32_e32 v64, 0x3f4c422a, v64
	v_add_f32_e32 v64, v64, v64
	v_pk_add_f32 v[62:63], v[62:63], 1.0 op_sel_hi:[1,0]
	v_mul_f32_e32 v64, 0x3fb8aa3b, v64
	v_exp_f32_e32 v64, v64
	v_pk_mul_f32 v[14:15], v[14:15], 0.5 op_sel_hi:[1,0]
	v_rcp_f32_e32 v63, v63
	s_nop 0
	v_add_f32_e32 v63, v63, v63
	v_mul_f32_e32 v65, 0x3d372713, v61
	v_mul_f32_e32 v65, v61, v65
	v_fma_f32 v65, v61, v65, v61
	v_mul_f32_e32 v65, 0x3f4c422a, v65
	v_add_f32_e32 v65, v65, v65
	v_mul_f32_e32 v65, 0x3fb8aa3b, v65
	v_exp_f32_e32 v65, v65
	v_rcp_f32_e32 v62, v62
	s_nop 0
	v_add_f32_e32 v62, v62, v62
	v_pk_add_f32 v[62:63], v[62:63], 1.0 op_sel_hi:[1,0] neg_lo:[1,0] neg_hi:[1,0]
	v_pk_add_f32 v[64:65], v[64:65], 1.0 op_sel_hi:[1,0]
	v_pk_add_f32 v[62:63], v[62:63], 1.0 op_sel_hi:[1,0]
	v_pk_mul_f32 v[62:63], v[14:15], v[62:63]
	v_pk_mul_f32 v[60:61], v[60:61], 0.5 op_sel_hi:[1,0]
	v_rcp_f32_e32 v15, v65
	s_nop 0
	v_add_f32_e32 v15, v15, v15
	v_rcp_f32_e32 v14, v64
	s_nop 0
	v_add_f32_e32 v14, v14, v14
	v_pk_add_f32 v[14:15], v[14:15], 1.0 op_sel_hi:[1,0] neg_lo:[1,0] neg_hi:[1,0]
	s_nop 0
	v_pk_add_f32 v[14:15], v[14:15], 1.0 op_sel_hi:[1,0]
	s_nop 0
	v_pk_mul_f32 v[60:61], v[60:61], v[14:15]
	v_cvt_pk_bf16_f32 v14, v16, v17
	v_cvt_pk_bf16_f32 v16, v58, v59
	v_or_b32_e32 v58, 0x2000, v12
	v_mov_b32_e32 v59, v13
	v_cvt_pk_bf16_f32 v15, v62, v63
	v_cvt_pk_bf16_f32 v17, v60, v61
	v_lshl_add_u64 v[58:59], v[86:87], 0, v[58:59]
	global_store_dwordx4 v[58:59], v[14:17], off
	v_or_b32_e32 v12, 0x3000, v12
	v_lshl_add_u64 v[12:13], v[86:87], 0, v[12:13]
	v_pk_fma_f32 v[16:17], v[54:55], s[20:21], v[6:7] op_sel_hi:[1,0,1]
	v_pk_fma_f32 v[14:15], v[56:57], s[20:21], v[8:9] op_sel_hi:[1,0,1]
	v_mul_f32_e32 v54, 0x3d372713, v16
	v_mul_f32_e32 v55, 0x3d372713, v17
	v_mul_f32_e32 v54, v16, v54
	v_mul_f32_e32 v55, v17, v55
	v_fma_f32 v54, v16, v54, v16
	v_fma_f32 v55, v17, v55, v17
	v_mul_f32_e32 v54, 0x3f4c422a, v54
	v_mul_f32_e32 v55, 0x3f4c422a, v55
	v_add_f32_e32 v54, v54, v54
	v_add_f32_e32 v55, v55, v55
	v_mul_f32_e32 v54, 0x3fb8aa3b, v54
	v_mul_f32_e32 v55, 0x3fb8aa3b, v55
	v_exp_f32_e32 v54, v54
	v_exp_f32_e32 v55, v55
	v_mul_f32_e32 v56, 0x3d372713, v50
	v_mul_f32_e32 v56, v50, v56
	v_fma_f32 v56, v50, v56, v50
	v_pk_add_f32 v[54:55], v[54:55], 1.0 op_sel_hi:[1,0]
	v_mul_f32_e32 v56, 0x3f4c422a, v56
	v_add_f32_e32 v56, v56, v56
	v_mul_f32_e32 v56, 0x3fb8aa3b, v56
	v_exp_f32_e32 v56, v56
	v_rcp_f32_e32 v55, v55
	s_nop 0
	v_add_f32_e32 v55, v55, v55
	v_pk_mul_f32 v[16:17], v[16:17], 0.5 op_sel_hi:[1,0]
	v_mul_f32_e32 v57, 0x3d372713, v51
	v_mul_f32_e32 v57, v51, v57
	v_fma_f32 v57, v51, v57, v51
	v_mul_f32_e32 v57, 0x3f4c422a, v57
	v_add_f32_e32 v57, v57, v57
	v_mul_f32_e32 v57, 0x3fb8aa3b, v57
	v_exp_f32_e32 v57, v57
	v_rcp_f32_e32 v54, v54
	s_nop 0
	v_add_f32_e32 v54, v54, v54
	v_pk_add_f32 v[54:55], v[54:55], 1.0 op_sel_hi:[1,0] neg_lo:[1,0] neg_hi:[1,0]
	v_pk_add_f32 v[56:57], v[56:57], 1.0 op_sel_hi:[1,0]
	v_pk_add_f32 v[54:55], v[54:55], 1.0 op_sel_hi:[1,0]
	v_pk_mul_f32 v[16:17], v[16:17], v[54:55]
	v_pk_mul_f32 v[50:51], v[50:51], 0.5 op_sel_hi:[1,0]
	v_rcp_f32_e32 v55, v57
	s_nop 0
	v_add_f32_e32 v55, v55, v55
	v_rcp_f32_e32 v54, v56
	s_nop 0
	v_add_f32_e32 v54, v54, v54
	v_pk_add_f32 v[54:55], v[54:55], 1.0 op_sel_hi:[1,0] neg_lo:[1,0] neg_hi:[1,0]
	v_mul_f32_e32 v56, 0x3d372713, v52
	v_pk_add_f32 v[54:55], v[54:55], 1.0 op_sel_hi:[1,0]
	v_mul_f32_e32 v56, v52, v56
	v_pk_mul_f32 v[50:51], v[50:51], v[54:55]
	v_mul_f32_e32 v54, 0x3d372713, v14
	v_mul_f32_e32 v55, 0x3d372713, v15
	v_mul_f32_e32 v54, v14, v54
	v_mul_f32_e32 v55, v15, v55
	v_fma_f32 v54, v14, v54, v14
	v_fma_f32 v55, v15, v55, v15
	v_mul_f32_e32 v54, 0x3f4c422a, v54
	v_mul_f32_e32 v55, 0x3f4c422a, v55
	v_add_f32_e32 v54, v54, v54
	v_add_f32_e32 v55, v55, v55
	v_mul_f32_e32 v54, 0x3fb8aa3b, v54
	v_mul_f32_e32 v55, 0x3fb8aa3b, v55
	v_exp_f32_e32 v54, v54
	v_exp_f32_e32 v55, v55
	v_fma_f32 v56, v52, v56, v52
	v_mul_f32_e32 v56, 0x3f4c422a, v56
	v_add_f32_e32 v56, v56, v56
	v_pk_add_f32 v[54:55], v[54:55], 1.0 op_sel_hi:[1,0]
	v_mul_f32_e32 v56, 0x3fb8aa3b, v56
	v_exp_f32_e32 v56, v56
	v_pk_mul_f32 v[14:15], v[14:15], 0.5 op_sel_hi:[1,0]
	v_rcp_f32_e32 v55, v55
	s_nop 0
	v_add_f32_e32 v55, v55, v55
	v_mul_f32_e32 v57, 0x3d372713, v53
	v_mul_f32_e32 v57, v53, v57
	v_fma_f32 v57, v53, v57, v53
	v_mul_f32_e32 v57, 0x3f4c422a, v57
	v_add_f32_e32 v57, v57, v57
	v_mul_f32_e32 v57, 0x3fb8aa3b, v57
	v_exp_f32_e32 v57, v57
	v_rcp_f32_e32 v54, v54
	s_nop 0
	v_add_f32_e32 v54, v54, v54
	v_pk_add_f32 v[54:55], v[54:55], 1.0 op_sel_hi:[1,0] neg_lo:[1,0] neg_hi:[1,0]
	v_pk_add_f32 v[56:57], v[56:57], 1.0 op_sel_hi:[1,0]
	v_pk_add_f32 v[54:55], v[54:55], 1.0 op_sel_hi:[1,0]
	v_pk_mul_f32 v[54:55], v[14:15], v[54:55]
	v_pk_mul_f32 v[52:53], v[52:53], 0.5 op_sel_hi:[1,0]
	v_rcp_f32_e32 v15, v57
	s_nop 0
	v_add_f32_e32 v15, v15, v15
	v_rcp_f32_e32 v14, v56
	s_nop 0
	v_add_f32_e32 v14, v14, v14
	v_pk_add_f32 v[14:15], v[14:15], 1.0 op_sel_hi:[1,0] neg_lo:[1,0] neg_hi:[1,0]
	s_nop 0
	v_pk_add_f32 v[14:15], v[14:15], 1.0 op_sel_hi:[1,0]
	s_nop 0
	v_pk_mul_f32 v[52:53], v[52:53], v[14:15]
	v_cvt_pk_bf16_f32 v14, v16, v17
	v_cvt_pk_bf16_f32 v15, v54, v55
	v_cvt_pk_bf16_f32 v16, v50, v51
	v_cvt_pk_bf16_f32 v17, v52, v53
	global_store_dwordx4 v[12:13], v[14:17], off
	v_pk_fma_f32 v[12:13], v[48:49], s[20:21], v[8:9] op_sel_hi:[1,0,1]
	s_nop 0
	v_pk_fma_f32 v[14:15], v[46:47], s[20:21], v[6:7] op_sel_hi:[1,0,1]
	v_pk_fma_f32 v[16:17], v[44:45], s[20:21], v[4:5] op_sel_hi:[1,0,1]
	v_mul_f32_e32 v44, 0x3d372713, v14
	v_mul_f32_e32 v45, 0x3d372713, v15
	v_mul_f32_e32 v44, v14, v44
	v_mul_f32_e32 v45, v15, v45
; __device__ __forceinline__ u32x4 pack8(const f32x4 v0, const f32x4 v1) { u32x4 w; w.x = cvt_pk_bf16(v0[0], v0[1]); w.y = cvt_pk_bf16(v0[2], v0[3]); w.z = cvt_pk_bf16(v1[0], v1[1]); w.w = cvt_pk_bf16(v1[2], v1[3]); return w; }
; #define EPI_ROWLOOP for (int ai = 0; ai < 2; ++ai) _Pragma("unroll") for (int m = 0; m < 4; ++m)
; __device__ __forceinline__ float gelu_tanh(float x) {
;     const float u = 0.7978845608028654f * (x + 0.044715f * x * x * x);
;     const float e = __expf(2.0f * u);
;     const float th = 1.0f - 2.0f / (e + 1.0f);
;     return 0.5f * x * (1.0f + th);
; }
;     __device__ __forceinline__ void operator()(const f32x4 (&acc)[2][2][4][2], const pg8::Unit& u, int wr, int wc, int fr, int fq) const {
;         const int row0 = u.pm * 256 + wr * 64 + fr, cl = wc * 32 + 8 * fq;
;         const f32x4 b0 = *(const f32x4*)(bias1 + u.pn * 128 + cl), b1 = *(const f32x4*)(bias1 + u.pn * 128 + cl + 4);
; #pragma unroll
;         EPI_ROWLOOP { f32x4 v0 = acc[ai][0][m][0] * (1.0f / (X8_SCALE * W8_SCALE)) + b0, v1 = acc[ai][0][m][1] * (1.0f / (X8_SCALE * W8_SCALE)) + b1;
; #pragma unroll
;             for (int i = 0; i < 4; ++i) { v0[i] = gelu_tanh(v0[i]); v1[i] = gelu_tanh(v1[i]); }
;             *(u32x4*)(CH1 + ((size_t)u.pn * 8192 + row0 + ai * 128 + m * 16) * 128 + cl) = pack8(v0, v1); }
;     }
	v_fma_f32 v44, v14, v44, v14
	v_fma_f32 v45, v15, v45, v15
	v_mul_f32_e32 v44, 0x3f4c422a, v44
	v_mul_f32_e32 v45, 0x3f4c422a, v45
	v_add_f32_e32 v44, v44, v44
	v_add_f32_e32 v45, v45, v45
	v_mul_f32_e32 v44, 0x3fb8aa3b, v44
	v_mul_f32_e32 v45, 0x3fb8aa3b, v45
	v_exp_f32_e32 v44, v44
	v_exp_f32_e32 v45, v45
	v_mul_f32_e32 v46, 0x3d372713, v42
	v_mul_f32_e32 v46, v42, v46
	v_fma_f32 v46, v42, v46, v42
	v_pk_add_f32 v[44:45], v[44:45], 1.0 op_sel_hi:[1,0]
	v_mul_f32_e32 v46, 0x3f4c422a, v46
	v_add_f32_e32 v46, v46, v46
	v_mul_f32_e32 v46, 0x3fb8aa3b, v46
	v_exp_f32_e32 v46, v46
	v_rcp_f32_e32 v45, v45
	s_nop 0
	v_add_f32_e32 v45, v45, v45
	v_pk_mul_f32 v[14:15], v[14:15], 0.5 op_sel_hi:[1,0]
	v_mul_f32_e32 v47, 0x3d372713, v43
	v_mul_f32_e32 v47, v43, v47
	v_fma_f32 v47, v43, v47, v43
	v_mul_f32_e32 v47, 0x3f4c422a, v47
	v_add_f32_e32 v47, v47, v47
	v_mul_f32_e32 v47, 0x3fb8aa3b, v47
	v_exp_f32_e32 v47, v47
	v_rcp_f32_e32 v44, v44
	s_nop 0
	v_add_f32_e32 v44, v44, v44
	v_pk_add_f32 v[44:45], v[44:45], 1.0 op_sel_hi:[1,0] neg_lo:[1,0] neg_hi:[1,0]
	v_pk_add_f32 v[46:47], v[46:47], 1.0 op_sel_hi:[1,0]
	v_pk_add_f32 v[44:45], v[44:45], 1.0 op_sel_hi:[1,0]
	v_pk_mul_f32 v[14:15], v[14:15], v[44:45]
	v_pk_mul_f32 v[42:43], v[42:43], 0.5 op_sel_hi:[1,0]
	v_cvt_pk_bf16_f32 v14, v14, v15
	v_rcp_f32_e32 v45, v47
	s_nop 0
	v_add_f32_e32 v45, v45, v45
	v_rcp_f32_e32 v44, v46
	s_nop 0
	v_add_f32_e32 v44, v44, v44
	v_pk_add_f32 v[44:45], v[44:45], 1.0 op_sel_hi:[1,0] neg_lo:[1,0] neg_hi:[1,0]
	v_mul_f32_e32 v46, 0x3d372713, v16
	v_pk_add_f32 v[44:45], v[44:45], 1.0 op_sel_hi:[1,0]
	v_mul_f32_e32 v46, v16, v46
	v_pk_mul_f32 v[42:43], v[42:43], v[44:45]
	v_mul_f32_e32 v44, 0x3d372713, v12
	v_mul_f32_e32 v45, 0x3d372713, v13
	v_mul_f32_e32 v44, v12, v44
	v_mul_f32_e32 v45, v13, v45
	v_fma_f32 v44, v12, v44, v12
	v_fma_f32 v45, v13, v45, v13
	v_mul_f32_e32 v44, 0x3f4c422a, v44
	v_mul_f32_e32 v45, 0x3f4c422a, v45
	v_add_f32_e32 v44, v44, v44
	v_add_f32_e32 v45, v45, v45
	v_mul_f32_e32 v44, 0x3fb8aa3b, v44
	v_mul_f32_e32 v45, 0x3fb8aa3b, v45
	v_exp_f32_e32 v44, v44
	v_exp_f32_e32 v45, v45
	v_fma_f32 v46, v16, v46, v16
	v_mul_f32_e32 v46, 0x3f4c422a, v46
	v_add_f32_e32 v46, v46, v46
	v_pk_add_f32 v[44:45], v[44:45], 1.0 op_sel_hi:[1,0]
	v_mul_f32_e32 v46, 0x3fb8aa3b, v46
	v_exp_f32_e32 v46, v46
	v_pk_mul_f32 v[12:13], v[12:13], 0.5 op_sel_hi:[1,0]
	v_rcp_f32_e32 v45, v45
	s_nop 0
	v_add_f32_e32 v45, v45, v45
	v_mul_f32_e32 v47, 0x3d372713, v17
	v_mul_f32_e32 v47, v17, v47
	v_fma_f32 v47, v17, v47, v17
	v_mul_f32_e32 v47, 0x3f4c422a, v47
	v_add_f32_e32 v47, v47, v47
	v_mul_f32_e32 v47, 0x3fb8aa3b, v47
	v_exp_f32_e32 v47, v47
	v_rcp_f32_e32 v44, v44
	s_nop 0
	v_add_f32_e32 v44, v44, v44
	v_pk_add_f32 v[44:45], v[44:45], 1.0 op_sel_hi:[1,0] neg_lo:[1,0] neg_hi:[1,0]
	v_pk_add_f32 v[46:47], v[46:47], 1.0 op_sel_hi:[1,0]
	v_pk_add_f32 v[44:45], v[44:45], 1.0 op_sel_hi:[1,0]
	v_pk_mul_f32 v[12:13], v[12:13], v[44:45]
	v_pk_mul_f32 v[16:17], v[16:17], 0.5 op_sel_hi:[1,0]
	v_cvt_pk_bf16_f32 v15, v12, v13
	v_rcp_f32_e32 v45, v47
	s_nop 0
	v_add_f32_e32 v45, v45, v45
	v_rcp_f32_e32 v44, v46
	s_nop 0
	v_add_f32_e32 v44, v44, v44
	v_pk_add_f32 v[44:45], v[44:45], 1.0 op_sel_hi:[1,0] neg_lo:[1,0] neg_hi:[1,0]
	v_add_co_u32_e32 v12, vcc, s50, v10
	v_pk_add_f32 v[44:45], v[44:45], 1.0 op_sel_hi:[1,0]
	s_nop 0
	v_addc_co_u32_e32 v13, vcc, 0, v11, vcc
	v_pk_mul_f32 v[44:45], v[16:17], v[44:45]
	v_cvt_pk_bf16_f32 v16, v42, v43
	v_cvt_pk_bf16_f32 v17, v44, v45
	global_store_dwordx4 v[12:13], v[14:17], off offset:-4096
	s_nop 1
	v_pk_fma_f32 v[16:17], v[38:39], s[20:21], v[6:7] op_sel_hi:[1,0,1]
	v_pk_fma_f32 v[14:15], v[40:41], s[20:21], v[8:9] op_sel_hi:[1,0,1]
	v_mul_f32_e32 v38, 0x3d372713, v16
	v_mul_f32_e32 v39, 0x3d372713, v17
	v_mul_f32_e32 v38, v16, v38
	v_mul_f32_e32 v39, v17, v39
	v_fma_f32 v38, v16, v38, v16
	v_fma_f32 v39, v17, v39, v17
	v_mul_f32_e32 v38, 0x3f4c422a, v38
	v_mul_f32_e32 v39, 0x3f4c422a, v39
	v_add_f32_e32 v38, v38, v38
	v_add_f32_e32 v39, v39, v39
	v_mul_f32_e32 v38, 0x3fb8aa3b, v38
	v_mul_f32_e32 v39, 0x3fb8aa3b, v39
	v_exp_f32_e32 v38, v38
	v_exp_f32_e32 v39, v39
	v_mul_f32_e32 v40, 0x3d372713, v34
	v_mul_f32_e32 v40, v34, v40
	v_fma_f32 v40, v34, v40, v34
	v_pk_add_f32 v[38:39], v[38:39], 1.0 op_sel_hi:[1,0]
	v_mul_f32_e32 v40, 0x3f4c422a, v40
	v_add_f32_e32 v40, v40, v40
	v_mul_f32_e32 v40, 0x3fb8aa3b, v40
	v_exp_f32_e32 v40, v40
	v_rcp_f32_e32 v39, v39
	s_nop 0
	v_add_f32_e32 v39, v39, v39
	v_pk_mul_f32 v[16:17], v[16:17], 0.5 op_sel_hi:[1,0]
	v_mul_f32_e32 v41, 0x3d372713, v35
	v_mul_f32_e32 v41, v35, v41
	v_fma_f32 v41, v35, v41, v35
	v_mul_f32_e32 v41, 0x3f4c422a, v41
	v_add_f32_e32 v41, v41, v41
	v_mul_f32_e32 v41, 0x3fb8aa3b, v41
	v_exp_f32_e32 v41, v41
	v_rcp_f32_e32 v38, v38
	s_nop 0
	v_add_f32_e32 v38, v38, v38
	v_pk_add_f32 v[38:39], v[38:39], 1.0 op_sel_hi:[1,0] neg_lo:[1,0] neg_hi:[1,0]
	v_pk_add_f32 v[40:41], v[40:41], 1.0 op_sel_hi:[1,0]
	v_pk_add_f32 v[38:39], v[38:39], 1.0 op_sel_hi:[1,0]
	v_pk_mul_f32 v[16:17], v[16:17], v[38:39]
	v_pk_mul_f32 v[34:35], v[34:35], 0.5 op_sel_hi:[1,0]
	v_rcp_f32_e32 v39, v41
	s_nop 0
	v_add_f32_e32 v39, v39, v39
	v_rcp_f32_e32 v38, v40
	s_nop 0
	v_add_f32_e32 v38, v38, v38
	v_pk_add_f32 v[38:39], v[38:39], 1.0 op_sel_hi:[1,0] neg_lo:[1,0] neg_hi:[1,0]
	v_mul_f32_e32 v40, 0x3d372713, v36
	v_pk_add_f32 v[38:39], v[38:39], 1.0 op_sel_hi:[1,0]
	v_mul_f32_e32 v40, v36, v40
	v_pk_mul_f32 v[34:35], v[34:35], v[38:39]
	v_mul_f32_e32 v38, 0x3d372713, v14
	v_mul_f32_e32 v39, 0x3d372713, v15
	v_mul_f32_e32 v38, v14, v38
	v_mul_f32_e32 v39, v15, v39
	v_fma_f32 v38, v14, v38, v14
	v_fma_f32 v39, v15, v39, v15
; __device__ __forceinline__ u32x4 pack8(const f32x4 v0, const f32x4 v1) { u32x4 w; w.x = cvt_pk_bf16(v0[0], v0[1]); w.y = cvt_pk_bf16(v0[2], v0[3]); w.z = cvt_pk_bf16(v1[0], v1[1]); w.w = cvt_pk_bf16(v1[2], v1[3]); return w; }
; #define EPI_ROWLOOP for (int ai = 0; ai < 2; ++ai) _Pragma("unroll") for (int m = 0; m < 4; ++m)
; __device__ __forceinline__ float gelu_tanh(float x) {
;     const float u = 0.7978845608028654f * (x + 0.044715f * x * x * x);
;     const float e = __expf(2.0f * u);
;     const float th = 1.0f - 2.0f / (e + 1.0f);
;     return 0.5f * x * (1.0f + th);
; }
;     __device__ __forceinline__ void operator()(const f32x4 (&acc)[2][2][4][2], const pg8::Unit& u, int wr, int wc, int fr, int fq) const {
;         const int row0 = u.pm * 256 + wr * 64 + fr, cl = wc * 32 + 8 * fq;
;         const f32x4 b0 = *(const f32x4*)(bias1 + u.pn * 128 + cl), b1 = *(const f32x4*)(bias1 + u.pn * 128 + cl + 4);
; #pragma unroll
;         EPI_ROWLOOP { f32x4 v0 = acc[ai][0][m][0] * (1.0f / (X8_SCALE * W8_SCALE)) + b0, v1 = acc[ai][0][m][1] * (1.0f / (X8_SCALE * W8_SCALE)) + b1;
; #pragma unroll
;             for (int i = 0; i < 4; ++i) { v0[i] = gelu_tanh(v0[i]); v1[i] = gelu_tanh(v1[i]); }
;             *(u32x4*)(CH1 + ((size_t)u.pn * 8192 + row0 + ai * 128 + m * 16) * 128 + cl) = pack8(v0, v1); }
;     }
	v_mul_f32_e32 v38, 0x3f4c422a, v38
	v_mul_f32_e32 v39, 0x3f4c422a, v39
	v_add_f32_e32 v38, v38, v38
	v_add_f32_e32 v39, v39, v39
	v_mul_f32_e32 v38, 0x3fb8aa3b, v38
	v_mul_f32_e32 v39, 0x3fb8aa3b, v39
	v_exp_f32_e32 v38, v38
	v_exp_f32_e32 v39, v39
	v_fma_f32 v40, v36, v40, v36
	v_mul_f32_e32 v40, 0x3f4c422a, v40
	v_add_f32_e32 v40, v40, v40
	v_pk_add_f32 v[38:39], v[38:39], 1.0 op_sel_hi:[1,0]
	v_mul_f32_e32 v40, 0x3fb8aa3b, v40
	v_exp_f32_e32 v40, v40
	v_pk_mul_f32 v[14:15], v[14:15], 0.5 op_sel_hi:[1,0]
	v_rcp_f32_e32 v39, v39
	s_nop 0
	v_add_f32_e32 v39, v39, v39
	v_mul_f32_e32 v41, 0x3d372713, v37
	v_mul_f32_e32 v41, v37, v41
	v_fma_f32 v41, v37, v41, v37
	v_mul_f32_e32 v41, 0x3f4c422a, v41
	v_add_f32_e32 v41, v41, v41
	v_mul_f32_e32 v41, 0x3fb8aa3b, v41
	v_exp_f32_e32 v41, v41
	v_rcp_f32_e32 v38, v38
	s_nop 0
	v_add_f32_e32 v38, v38, v38
	v_pk_add_f32 v[38:39], v[38:39], 1.0 op_sel_hi:[1,0] neg_lo:[1,0] neg_hi:[1,0]
	v_pk_add_f32 v[40:41], v[40:41], 1.0 op_sel_hi:[1,0]
	v_pk_add_f32 v[38:39], v[38:39], 1.0 op_sel_hi:[1,0]
	v_pk_mul_f32 v[38:39], v[14:15], v[38:39]
	v_pk_mul_f32 v[36:37], v[36:37], 0.5 op_sel_hi:[1,0]
	v_rcp_f32_e32 v15, v41
	s_nop 0
	v_add_f32_e32 v15, v15, v15
	v_rcp_f32_e32 v14, v40
	s_nop 0
	v_add_f32_e32 v14, v14, v14
	v_pk_add_f32 v[14:15], v[14:15], 1.0 op_sel_hi:[1,0] neg_lo:[1,0] neg_hi:[1,0]
	s_nop 0
	v_pk_add_f32 v[14:15], v[14:15], 1.0 op_sel_hi:[1,0]
	s_nop 0
	v_pk_mul_f32 v[36:37], v[36:37], v[14:15]
	v_cvt_pk_bf16_f32 v14, v16, v17
	v_cvt_pk_bf16_f32 v15, v38, v39
	v_cvt_pk_bf16_f32 v16, v34, v35
	v_cvt_pk_bf16_f32 v17, v36, v37
	global_store_dwordx4 v[12:13], v[14:17], off
	v_pk_fma_f32 v[12:13], v[32:33], s[20:21], v[8:9] op_sel_hi:[1,0,1]
	v_pk_fma_f32 v[8:9], v[24:25], s[20:21], v[8:9] op_sel_hi:[1,0,1]
	v_pk_fma_f32 v[14:15], v[30:31], s[20:21], v[6:7] op_sel_hi:[1,0,1]
	v_pk_fma_f32 v[16:17], v[28:29], s[20:21], v[4:5] op_sel_hi:[1,0,1]
	v_mul_f32_e32 v28, 0x3d372713, v14
	v_mul_f32_e32 v29, 0x3d372713, v15
	v_mul_f32_e32 v28, v14, v28
	v_mul_f32_e32 v29, v15, v29
	v_fma_f32 v28, v14, v28, v14
	v_fma_f32 v29, v15, v29, v15
	v_mul_f32_e32 v28, 0x3f4c422a, v28
	v_mul_f32_e32 v29, 0x3f4c422a, v29
	v_add_f32_e32 v28, v28, v28
	v_add_f32_e32 v29, v29, v29
	v_mul_f32_e32 v28, 0x3fb8aa3b, v28
	v_mul_f32_e32 v29, 0x3fb8aa3b, v29
	v_exp_f32_e32 v28, v28
	v_exp_f32_e32 v29, v29
	v_mul_f32_e32 v30, 0x3d372713, v26
	v_mul_f32_e32 v30, v26, v30
	v_fma_f32 v30, v26, v30, v26
	v_pk_add_f32 v[28:29], v[28:29], 1.0 op_sel_hi:[1,0]
	v_mul_f32_e32 v30, 0x3f4c422a, v30
	v_add_f32_e32 v30, v30, v30
	v_mul_f32_e32 v30, 0x3fb8aa3b, v30
	v_exp_f32_e32 v30, v30
	v_rcp_f32_e32 v29, v29
	s_nop 0
	v_add_f32_e32 v29, v29, v29
	v_pk_mul_f32 v[14:15], v[14:15], 0.5 op_sel_hi:[1,0]
	v_mul_f32_e32 v31, 0x3d372713, v27
	v_mul_f32_e32 v31, v27, v31
	v_fma_f32 v31, v27, v31, v27
	v_mul_f32_e32 v31, 0x3f4c422a, v31
	v_add_f32_e32 v31, v31, v31
	v_mul_f32_e32 v31, 0x3fb8aa3b, v31
	v_exp_f32_e32 v31, v31
	v_rcp_f32_e32 v28, v28
	s_nop 0
	v_add_f32_e32 v28, v28, v28
	v_pk_add_f32 v[28:29], v[28:29], 1.0 op_sel_hi:[1,0] neg_lo:[1,0] neg_hi:[1,0]
	v_pk_add_f32 v[30:31], v[30:31], 1.0 op_sel_hi:[1,0]
	v_pk_add_f32 v[28:29], v[28:29], 1.0 op_sel_hi:[1,0]
	v_pk_mul_f32 v[14:15], v[14:15], v[28:29]
	v_pk_mul_f32 v[26:27], v[26:27], 0.5 op_sel_hi:[1,0]
	v_pk_fma_f32 v[6:7], v[22:23], s[20:21], v[6:7] op_sel_hi:[1,0,1]
	v_rcp_f32_e32 v29, v31
	s_nop 0
	v_add_f32_e32 v29, v29, v29
	v_pk_fma_f32 v[4:5], v[20:21], s[20:21], v[4:5] op_sel_hi:[1,0,1]
	v_rcp_f32_e32 v28, v30
	s_nop 0
	v_add_f32_e32 v28, v28, v28
	v_pk_add_f32 v[28:29], v[28:29], 1.0 op_sel_hi:[1,0] neg_lo:[1,0] neg_hi:[1,0]
	v_mul_f32_e32 v30, 0x3d372713, v16
	v_pk_add_f32 v[28:29], v[28:29], 1.0 op_sel_hi:[1,0]
	v_mul_f32_e32 v30, v16, v30
	v_pk_mul_f32 v[26:27], v[26:27], v[28:29]
	v_mul_f32_e32 v28, 0x3d372713, v12
	v_mul_f32_e32 v29, 0x3d372713, v13
	v_mul_f32_e32 v28, v12, v28
	v_mul_f32_e32 v29, v13, v29
	v_fma_f32 v28, v12, v28, v12
	v_fma_f32 v29, v13, v29, v13
	v_mul_f32_e32 v28, 0x3f4c422a, v28
	v_mul_f32_e32 v29, 0x3f4c422a, v29
	v_add_f32_e32 v28, v28, v28
	v_add_f32_e32 v29, v29, v29
	v_mul_f32_e32 v28, 0x3fb8aa3b, v28
	v_mul_f32_e32 v29, 0x3fb8aa3b, v29
	v_exp_f32_e32 v28, v28
	v_exp_f32_e32 v29, v29
	v_fma_f32 v30, v16, v30, v16
	v_mul_f32_e32 v30, 0x3f4c422a, v30
	v_add_f32_e32 v30, v30, v30
	v_pk_add_f32 v[28:29], v[28:29], 1.0 op_sel_hi:[1,0]
	v_mul_f32_e32 v30, 0x3fb8aa3b, v30
	v_exp_f32_e32 v30, v30
	v_pk_mul_f32 v[12:13], v[12:13], 0.5 op_sel_hi:[1,0]
	v_rcp_f32_e32 v29, v29
	s_nop 0
	v_add_f32_e32 v29, v29, v29
	v_mul_f32_e32 v31, 0x3d372713, v17
	v_mul_f32_e32 v31, v17, v31
	v_fma_f32 v31, v17, v31, v17
	v_mul_f32_e32 v31, 0x3f4c422a, v31
	v_add_f32_e32 v31, v31, v31
; __device__ __forceinline__ u32x4 pack8(const f32x4 v0, const f32x4 v1) { u32x4 w; w.x = cvt_pk_bf16(v0[0], v0[1]); w.y = cvt_pk_bf16(v0[2], v0[3]); w.z = cvt_pk_bf16(v1[0], v1[1]); w.w = cvt_pk_bf16(v1[2], v1[3]); return w; }
; #define EPI_ROWLOOP for (int ai = 0; ai < 2; ++ai) _Pragma("unroll") for (int m = 0; m < 4; ++m)
; __device__ __forceinline__ float gelu_tanh(float x) {
;     const float u = 0.7978845608028654f * (x + 0.044715f * x * x * x);
;     const float e = __expf(2.0f * u);
;     const float th = 1.0f - 2.0f / (e + 1.0f);
;     return 0.5f * x * (1.0f + th);
; }
;     __device__ __forceinline__ void operator()(const f32x4 (&acc)[2][2][4][2], const pg8::Unit& u, int wr, int wc, int fr, int fq) const {
;         const int row0 = u.pm * 256 + wr * 64 + fr, cl = wc * 32 + 8 * fq;
;         const f32x4 b0 = *(const f32x4*)(bias1 + u.pn * 128 + cl), b1 = *(const f32x4*)(bias1 + u.pn * 128 + cl + 4);
; #pragma unroll
;         EPI_ROWLOOP { f32x4 v0 = acc[ai][0][m][0] * (1.0f / (X8_SCALE * W8_SCALE)) + b0, v1 = acc[ai][0][m][1] * (1.0f / (X8_SCALE * W8_SCALE)) + b1;
; #pragma unroll
;             for (int i = 0; i < 4; ++i) { v0[i] = gelu_tanh(v0[i]); v1[i] = gelu_tanh(v1[i]); }
;             *(u32x4*)(CH1 + ((size_t)u.pn * 8192 + row0 + ai * 128 + m * 16) * 128 + cl) = pack8(v0, v1); }
;     }
	v_mul_f32_e32 v31, 0x3fb8aa3b, v31
	v_exp_f32_e32 v31, v31
	v_rcp_f32_e32 v28, v28
	s_nop 0
	v_add_f32_e32 v28, v28, v28
	v_pk_add_f32 v[28:29], v[28:29], 1.0 op_sel_hi:[1,0] neg_lo:[1,0] neg_hi:[1,0]
	v_pk_add_f32 v[30:31], v[30:31], 1.0 op_sel_hi:[1,0]
	v_pk_add_f32 v[28:29], v[28:29], 1.0 op_sel_hi:[1,0]
	v_pk_mul_f32 v[28:29], v[12:13], v[28:29]
	v_pk_mul_f32 v[16:17], v[16:17], 0.5 op_sel_hi:[1,0]
	v_rcp_f32_e32 v13, v31
	s_nop 0
	v_add_f32_e32 v13, v13, v13
	v_rcp_f32_e32 v12, v30
	s_nop 0
	v_add_f32_e32 v12, v12, v12
	v_pk_add_f32 v[12:13], v[12:13], 1.0 op_sel_hi:[1,0] neg_lo:[1,0] neg_hi:[1,0]
	s_nop 0
	v_pk_add_f32 v[12:13], v[12:13], 1.0 op_sel_hi:[1,0]
	s_nop 0
	v_pk_mul_f32 v[16:17], v[16:17], v[12:13]
	v_cvt_pk_bf16_f32 v12, v14, v15
	v_cvt_pk_bf16_f32 v15, v16, v17
	v_add_co_u32_e32 v16, vcc, s47, v10
	v_cvt_pk_bf16_f32 v13, v28, v29
	v_cvt_pk_bf16_f32 v14, v26, v27
	v_addc_co_u32_e32 v17, vcc, 0, v11, vcc
	global_store_dwordx4 v[16:17], v[12:15], off
	s_nop 1
	v_mul_f32_e32 v12, 0x3d372713, v6
	v_mul_f32_e32 v13, 0x3d372713, v7
	v_mul_f32_e32 v12, v6, v12
	v_mul_f32_e32 v13, v7, v13
	v_fma_f32 v12, v6, v12, v6
	v_fma_f32 v13, v7, v13, v7
	v_mul_f32_e32 v12, 0x3f4c422a, v12
	v_mul_f32_e32 v13, 0x3f4c422a, v13
	v_add_f32_e32 v12, v12, v12
	v_add_f32_e32 v13, v13, v13
	v_mul_f32_e32 v12, 0x3fb8aa3b, v12
	v_mul_f32_e32 v13, 0x3fb8aa3b, v13
	v_exp_f32_e32 v12, v12
	v_exp_f32_e32 v13, v13
	v_mul_f32_e32 v14, 0x3d372713, v2
	v_mul_f32_e32 v14, v2, v14
	v_fma_f32 v14, v2, v14, v2
	v_pk_add_f32 v[12:13], v[12:13], 1.0 op_sel_hi:[1,0]
	v_mul_f32_e32 v14, 0x3f4c422a, v14
	v_add_f32_e32 v14, v14, v14
	v_mul_f32_e32 v14, 0x3fb8aa3b, v14
	v_exp_f32_e32 v14, v14
	v_rcp_f32_e32 v13, v13
	s_nop 0
	v_add_f32_e32 v13, v13, v13
	v_pk_mul_f32 v[6:7], v[6:7], 0.5 op_sel_hi:[1,0]
	v_mul_f32_e32 v15, 0x3d372713, v3
	v_mul_f32_e32 v15, v3, v15
	v_fma_f32 v15, v3, v15, v3
	v_mul_f32_e32 v15, 0x3f4c422a, v15
	v_add_f32_e32 v15, v15, v15
	v_mul_f32_e32 v15, 0x3fb8aa3b, v15
	v_exp_f32_e32 v15, v15
	v_rcp_f32_e32 v12, v12
	s_nop 0
	v_add_f32_e32 v12, v12, v12
	v_pk_add_f32 v[12:13], v[12:13], 1.0 op_sel_hi:[1,0] neg_lo:[1,0] neg_hi:[1,0]
	v_pk_add_f32 v[14:15], v[14:15], 1.0 op_sel_hi:[1,0]
	v_pk_add_f32 v[12:13], v[12:13], 1.0 op_sel_hi:[1,0]
	v_pk_mul_f32 v[6:7], v[6:7], v[12:13]
	v_pk_mul_f32 v[2:3], v[2:3], 0.5 op_sel_hi:[1,0]
	v_rcp_f32_e32 v13, v15
	s_nop 0
	v_add_f32_e32 v13, v13, v13
	v_rcp_f32_e32 v12, v14
	s_nop 0
	v_add_f32_e32 v12, v12, v12
	v_pk_add_f32 v[12:13], v[12:13], 1.0 op_sel_hi:[1,0] neg_lo:[1,0] neg_hi:[1,0]
	v_mul_f32_e32 v14, 0x3d372713, v4
	v_pk_add_f32 v[12:13], v[12:13], 1.0 op_sel_hi:[1,0]
	v_mul_f32_e32 v14, v4, v14
	v_pk_mul_f32 v[12:13], v[2:3], v[12:13]
	v_mul_f32_e32 v2, 0x3d372713, v8
	v_mul_f32_e32 v3, 0x3d372713, v9
	v_mul_f32_e32 v2, v8, v2
	v_mul_f32_e32 v3, v9, v3
	v_fma_f32 v2, v8, v2, v8
	v_fma_f32 v3, v9, v3, v9
	v_mul_f32_e32 v2, 0x3f4c422a, v2
	v_mul_f32_e32 v3, 0x3f4c422a, v3
	v_add_f32_e32 v2, v2, v2
	v_add_f32_e32 v3, v3, v3
	v_mul_f32_e32 v2, 0x3fb8aa3b, v2
	v_mul_f32_e32 v3, 0x3fb8aa3b, v3
	v_exp_f32_e32 v2, v2
	v_exp_f32_e32 v3, v3
	v_fma_f32 v14, v4, v14, v4
	v_mul_f32_e32 v14, 0x3f4c422a, v14
	v_add_f32_e32 v14, v14, v14
	v_pk_add_f32 v[2:3], v[2:3], 1.0 op_sel_hi:[1,0]
	v_mul_f32_e32 v14, 0x3fb8aa3b, v14
	v_exp_f32_e32 v14, v14
	v_pk_mul_f32 v[8:9], v[8:9], 0.5 op_sel_hi:[1,0]
	v_rcp_f32_e32 v3, v3
	s_nop 0
	v_add_f32_e32 v3, v3, v3
	v_mul_f32_e32 v15, 0x3d372713, v5
	v_mul_f32_e32 v15, v5, v15
	v_fma_f32 v15, v5, v15, v5
	v_mul_f32_e32 v15, 0x3f4c422a, v15
	v_add_f32_e32 v15, v15, v15
	v_mul_f32_e32 v15, 0x3fb8aa3b, v15
	v_exp_f32_e32 v15, v15
	v_rcp_f32_e32 v2, v2
	s_nop 0
	v_add_f32_e32 v2, v2, v2
	v_pk_add_f32 v[2:3], v[2:3], 1.0 op_sel_hi:[1,0] neg_lo:[1,0] neg_hi:[1,0]
	v_pk_add_f32 v[14:15], v[14:15], 1.0 op_sel_hi:[1,0]
	v_pk_add_f32 v[2:3], v[2:3], 1.0 op_sel_hi:[1,0]
	v_pk_mul_f32 v[8:9], v[8:9], v[2:3]
	v_pk_mul_f32 v[4:5], v[4:5], 0.5 op_sel_hi:[1,0]
	v_rcp_f32_e32 v3, v15
	s_nop 0
	v_add_f32_e32 v3, v3, v3
	s_mov_b64 s[0:1], -1
	v_rcp_f32_e32 v2, v14
	s_nop 0
	v_add_f32_e32 v2, v2, v2
	v_pk_add_f32 v[2:3], v[2:3], 1.0 op_sel_hi:[1,0] neg_lo:[1,0] neg_hi:[1,0]
	s_nop 0
	v_pk_add_f32 v[2:3], v[2:3], 1.0 op_sel_hi:[1,0]
	s_nop 0
	v_pk_mul_f32 v[14:15], v[4:5], v[2:3]
	v_cvt_pk_bf16_f32 v2, v6, v7
	v_add_co_u32_e32 v6, vcc, 0xb000, v10
	v_cvt_pk_bf16_f32 v3, v8, v9
	v_cvt_pk_bf16_f32 v4, v12, v13
	v_cvt_pk_bf16_f32 v5, v14, v15
	v_addc_co_u32_e32 v7, vcc, 0, v11, vcc
	global_store_dwordx4 v[6:7], v[2:5], off
	s_load_dwordx2 s[58:59], s[82:83], 0x118
	s_andn2_b64 vcc, exec, s[22:23]
	s_cbranch_vccnz .LBB0_1427
	s_andn2_b64 vcc, exec, s[10:11]
	s_cbranch_vccnz .LBB0_1426
	s_barrier
	s_branch .LBB0_1426

; __device__ __forceinline__ u32x4 pack8(const f32x4 v0, const f32x4 v1) { u32x4 w; w.x = cvt_pk_bf16(v0[0], v0[1]); w.y = cvt_pk_bf16(v0[2], v0[3]); w.z = cvt_pk_bf16(v1[0], v1[1]); w.w = cvt_pk_bf16(v1[2], v1[3]); return w; }
; #define EPI_ROWLOOP for (int ai = 0; ai < 2; ++ai) _Pragma("unroll") for (int m = 0; m < 4; ++m)
;     __device__ __forceinline__ void operator()(const f32x4 (&acc)[2][2][4][2], const pg8::Unit& u, int wr, int wc, int fr, int fq) const {
;         const int row0 = u.pm * 256 + wr * 64 + fr, c0 = u.pn * 256 + wc * 32 + 8 * fq;
; #pragma unroll
;         EPI_ROWLOOP { const size_t ro = (size_t)(row0 + ai * 128 + m * 16) * 1024 + c0;
; #pragma unroll
;             for (int bj = 0; bj < 2; ++bj) {
;                 f32x4 r0, r1;
;                 if (resf) { r0 = *(const f32x4*)(resf + ro + bj * 128); r1 = *(const f32x4*)(resf + ro + bj * 128 + 4); }
;                 else { const u32x4 xv = *(const u32x4*)(resb + ro + bj * 128);
;                     r0[0] = __uint_as_float(xv.x << 16); r0[1] = __uint_as_float(xv.x & 0xffff0000u); r0[2] = __uint_as_float(xv.y << 16); r0[3] = __uint_as_float(xv.y & 0xffff0000u);
;                     r1[0] = __uint_as_float(xv.z << 16); r1[1] = __uint_as_float(xv.z & 0xffff0000u); r1[2] = __uint_as_float(xv.w << 16); r1[3] = __uint_as_float(xv.w & 0xffff0000u); }
;                 *(u32x4*)(Y + ro + bj * 128) = pack8(acc[ai][bj][m][0] * sc + r0 * ALPHA, acc[ai][bj][m][1] * sc + r1 * ALPHA);
;             } }
;     }
.LBB0_2363:
	v_lshl_add_u32 v6, s59, 8, v169
	v_lshl_or_b32 v4, s62, 8, v170
	v_ashrrev_i32_e32 v7, 31, v6
	v_ashrrev_i32_e32 v5, 31, v4
	v_lshlrev_b64 v[2:3], 10, v[6:7]
	v_lshl_add_u64 v[2:3], v[2:3], 0, v[4:5]
	v_lshlrev_b64 v[2:3], 1, v[2:3]
	v_lshl_add_u64 v[12:13], s[6:7], 0, v[2:3]
	global_load_dwordx4 v[8:11], v[12:13], off
	s_nop 0
	global_load_dwordx4 v[12:15], v[12:13], off offset:256
	s_add_u32 s98, s6, 0x8000
	s_addc_u32 s99, s7, 0
	global_load_dwordx4 v[176:179], v2, s[98:99]
	global_load_dwordx4 v[180:183], v2, s[98:99] offset:256
	s_add_u32 s98, s6, 0x10000
	s_addc_u32 s99, s7, 0
	global_load_dwordx4 v[184:187], v2, s[98:99]
	global_load_dwordx4 v[188:191], v2, s[98:99] offset:256
	s_add_u32 s98, s6, 0x18000
	s_addc_u32 s99, s7, 0
	global_load_dwordx4 v[192:195], v2, s[98:99]
	global_load_dwordx4 v[196:199], v2, s[98:99] offset:256
	s_add_u32 s98, s6, s16
	s_addc_u32 s99, s7, s17
	global_load_dwordx4 v[200:203], v2, s[98:99]
	global_load_dwordx4 v[204:207], v2, s[98:99] offset:256
	s_add_u32 s98, s6, s18
	s_addc_u32 s99, s7, s19
	global_load_dwordx4 v[224:227], v2, s[98:99]
	global_load_dwordx4 v[228:231], v2, s[98:99] offset:256
	s_add_u32 s98, s6, s20
	s_addc_u32 s99, s7, s21
	global_load_dwordx4 v[232:235], v2, s[98:99]
	global_load_dwordx4 v[236:239], v2, s[98:99] offset:256
	s_add_u32 s98, s6, s22
	s_addc_u32 s99, s7, s23
	global_load_dwordx4 v[240:243], v2, s[98:99]
	global_load_dwordx4 v[244:247], v2, s[98:99] offset:256
	v_or_b32_e32 v16, 16, v6
	v_ashrrev_i32_e32 v17, 31, v16
	v_lshlrev_b64 v[16:17], 10, v[16:17]
	v_lshl_add_u64 v[16:17], v[16:17], 0, v[4:5]
	v_lshl_add_u64 v[18:19], s[8:9], 0, v[2:3]
	v_lshlrev_b64 v[16:17], 1, v[16:17]
	v_lshl_add_u64 v[20:21], s[6:7], 0, v[16:17]
	v_lshl_add_u64 v[16:17], s[8:9], 0, v[16:17]
	s_andn2_b64 vcc, exec, s[4:5]
	s_mov_b64 s[4:5], -1
	s_waitcnt vmcnt(14)
	v_lshlrev_b32_e32 v22, 16, v8
	v_and_b32_e32 v23, 0xffff0000, v8
	v_lshlrev_b32_e32 v8, 16, v9
	v_and_b32_e32 v9, 0xffff0000, v9
	v_lshlrev_b32_e32 v24, 16, v10
	v_and_b32_e32 v25, 0xffff0000, v10
	v_lshlrev_b32_e32 v10, 16, v11
	v_and_b32_e32 v11, 0xffff0000, v11
	v_lshlrev_b32_e32 v26, 16, v12
	v_and_b32_e32 v27, 0xffff0000, v12
	v_lshlrev_b32_e32 v12, 16, v13
	v_and_b32_e32 v13, 0xffff0000, v13
	v_lshlrev_b32_e32 v28, 16, v14
	v_and_b32_e32 v29, 0xffff0000, v14
	v_lshlrev_b32_e32 v14, 16, v15
	v_and_b32_e32 v15, 0xffff0000, v15
	v_pk_mul_f32 v[22:23], v[22:23], s[12:13] op_sel_hi:[1,0]
	v_pk_mul_f32 v[8:9], v[8:9], s[12:13] op_sel_hi:[1,0]
	v_pk_mul_f32 v[24:25], v[24:25], s[12:13] op_sel_hi:[1,0]
	v_pk_mul_f32 v[10:11], v[10:11], s[12:13] op_sel_hi:[1,0]
	v_pk_mul_f32 v[26:27], v[26:27], s[12:13] op_sel_hi:[1,0]
	v_pk_mul_f32 v[12:13], v[12:13], s[12:13] op_sel_hi:[1,0]
	v_pk_mul_f32 v[28:29], v[28:29], s[12:13] op_sel_hi:[1,0]
	v_pk_mul_f32 v[14:15], v[14:15], s[12:13] op_sel_hi:[1,0]
	v_pk_fma_f32 v[30:31], v[160:161], s[14:15], v[8:9] op_sel_hi:[1,0,1]
	v_pk_fma_f32 v[8:9], v[158:159], s[14:15], v[22:23] op_sel_hi:[1,0,1]
	v_pk_fma_f32 v[22:23], v[156:157], s[14:15], v[10:11] op_sel_hi:[1,0,1]
	v_pk_fma_f32 v[10:11], v[154:155], s[14:15], v[24:25] op_sel_hi:[1,0,1]
	v_pk_fma_f32 v[24:25], v[152:153], s[14:15], v[12:13] op_sel_hi:[1,0,1]
	v_pk_fma_f32 v[12:13], v[150:151], s[14:15], v[26:27] op_sel_hi:[1,0,1]
	v_pk_fma_f32 v[26:27], v[148:149], s[14:15], v[14:15] op_sel_hi:[1,0,1]
	v_pk_fma_f32 v[14:15], v[146:147], s[14:15], v[28:29] op_sel_hi:[1,0,1]
	v_cvt_pk_bf16_f32 v8, v8, v9
	v_cvt_pk_bf16_f32 v9, v30, v31
	v_cvt_pk_bf16_f32 v10, v10, v11
	v_cvt_pk_bf16_f32 v11, v22, v23
	v_cvt_pk_bf16_f32 v12, v12, v13
	v_cvt_pk_bf16_f32 v13, v24, v25
	v_cvt_pk_bf16_f32 v14, v14, v15
	v_cvt_pk_bf16_f32 v15, v26, v27
	global_store_dwordx4 v[18:19], v[8:11], off
	global_store_dwordx4 v[18:19], v[12:15], off offset:256
	s_nop 1
	s_waitcnt vmcnt(14)
	v_mov_b32_e32 v8, v176
	v_mov_b32_e32 v9, v177
	v_mov_b32_e32 v10, v178
	v_mov_b32_e32 v11, v179
	v_mov_b32_e32 v12, v180
	v_mov_b32_e32 v13, v181
	v_mov_b32_e32 v14, v182
	v_mov_b32_e32 v15, v183
	v_or_b32_e32 v18, 32, v6
	v_ashrrev_i32_e32 v19, 31, v18
	v_lshlrev_b64 v[18:19], 10, v[18:19]
	v_lshl_add_u64 v[18:19], v[18:19], 0, v[4:5]
	v_lshlrev_b64 v[18:19], 1, v[18:19]
	v_lshl_add_u64 v[20:21], s[6:7], 0, v[18:19]
	v_or_b32_e32 v6, 48, v6
	v_ashrrev_i32_e32 v7, 31, v6
	v_lshlrev_b64 v[6:7], 10, v[6:7]
	v_lshl_add_u64 v[4:5], v[6:7], 0, v[4:5]
	v_lshl_add_u64 v[18:19], s[8:9], 0, v[18:19]
	v_lshlrev_b32_e32 v22, 16, v8
	v_and_b32_e32 v23, 0xffff0000, v8
	v_lshlrev_b32_e32 v8, 16, v9
	v_and_b32_e32 v9, 0xffff0000, v9
	v_lshlrev_b32_e32 v24, 16, v10
	v_and_b32_e32 v25, 0xffff0000, v10
	v_lshlrev_b32_e32 v10, 16, v11
	v_and_b32_e32 v11, 0xffff0000, v11
	v_lshlrev_b32_e32 v26, 16, v12
	v_and_b32_e32 v27, 0xffff0000, v12
	v_lshlrev_b32_e32 v12, 16, v13
	v_and_b32_e32 v13, 0xffff0000, v13
	v_lshlrev_b32_e32 v28, 16, v14
	v_and_b32_e32 v29, 0xffff0000, v14
	v_lshlrev_b32_e32 v14, 16, v15
	v_and_b32_e32 v15, 0xffff0000, v15
	v_pk_mul_f32 v[22:23], v[22:23], s[12:13] op_sel_hi:[1,0]
	v_pk_mul_f32 v[8:9], v[8:9], s[12:13] op_sel_hi:[1,0]
	v_pk_mul_f32 v[24:25], v[24:25], s[12:13] op_sel_hi:[1,0]
	v_pk_mul_f32 v[10:11], v[10:11], s[12:13] op_sel_hi:[1,0]
	v_pk_mul_f32 v[26:27], v[26:27], s[12:13] op_sel_hi:[1,0]
	v_pk_mul_f32 v[12:13], v[12:13], s[12:13] op_sel_hi:[1,0]
	v_pk_mul_f32 v[28:29], v[28:29], s[12:13] op_sel_hi:[1,0]
	v_pk_mul_f32 v[14:15], v[14:15], s[12:13] op_sel_hi:[1,0]
	v_pk_fma_f32 v[30:31], v[144:145], s[14:15], v[8:9] op_sel_hi:[1,0,1]
	v_pk_fma_f32 v[8:9], v[142:143], s[14:15], v[22:23] op_sel_hi:[1,0,1]
	v_pk_fma_f32 v[22:23], v[140:141], s[14:15], v[10:11] op_sel_hi:[1,0,1]
	v_pk_fma_f32 v[10:11], v[138:139], s[14:15], v[24:25] op_sel_hi:[1,0,1]
	v_pk_fma_f32 v[24:25], v[136:137], s[14:15], v[12:13] op_sel_hi:[1,0,1]
	v_pk_fma_f32 v[12:13], v[134:135], s[14:15], v[26:27] op_sel_hi:[1,0,1]
	v_pk_fma_f32 v[26:27], v[132:133], s[14:15], v[14:15] op_sel_hi:[1,0,1]
	v_pk_fma_f32 v[14:15], v[130:131], s[14:15], v[28:29] op_sel_hi:[1,0,1]
	v_cvt_pk_bf16_f32 v8, v8, v9
	v_cvt_pk_bf16_f32 v9, v30, v31
	v_cvt_pk_bf16_f32 v10, v10, v11
	v_cvt_pk_bf16_f32 v11, v22, v23
	v_cvt_pk_bf16_f32 v12, v12, v13
	v_cvt_pk_bf16_f32 v13, v24, v25
	v_cvt_pk_bf16_f32 v14, v14, v15
	v_cvt_pk_bf16_f32 v15, v26, v27
	global_store_dwordx4 v[16:17], v[8:11], off
	global_store_dwordx4 v[16:17], v[12:15], off offset:256
	s_nop 1
	s_waitcnt vmcnt(14)
; __device__ __forceinline__ u32x4 pack8(const f32x4 v0, const f32x4 v1) { u32x4 w; w.x = cvt_pk_bf16(v0[0], v0[1]); w.y = cvt_pk_bf16(v0[2], v0[3]); w.z = cvt_pk_bf16(v1[0], v1[1]); w.w = cvt_pk_bf16(v1[2], v1[3]); return w; }
; #define EPI_ROWLOOP for (int ai = 0; ai < 2; ++ai) _Pragma("unroll") for (int m = 0; m < 4; ++m)
;     __device__ __forceinline__ void operator()(const f32x4 (&acc)[2][2][4][2], const pg8::Unit& u, int wr, int wc, int fr, int fq) const {
;         const int row0 = u.pm * 256 + wr * 64 + fr, c0 = u.pn * 256 + wc * 32 + 8 * fq;
; #pragma unroll
;         EPI_ROWLOOP { const size_t ro = (size_t)(row0 + ai * 128 + m * 16) * 1024 + c0;
; #pragma unroll
;             for (int bj = 0; bj < 2; ++bj) {
;                 f32x4 r0, r1;
;                 if (resf) { r0 = *(const f32x4*)(resf + ro + bj * 128); r1 = *(const f32x4*)(resf + ro + bj * 128 + 4); }
;                 else { const u32x4 xv = *(const u32x4*)(resb + ro + bj * 128);
;                     r0[0] = __uint_as_float(xv.x << 16); r0[1] = __uint_as_float(xv.x & 0xffff0000u); r0[2] = __uint_as_float(xv.y << 16); r0[3] = __uint_as_float(xv.y & 0xffff0000u);
;                     r1[0] = __uint_as_float(xv.z << 16); r1[1] = __uint_as_float(xv.z & 0xffff0000u); r1[2] = __uint_as_float(xv.w << 16); r1[3] = __uint_as_float(xv.w & 0xffff0000u); }
;                 *(u32x4*)(Y + ro + bj * 128) = pack8(acc[ai][bj][m][0] * sc + r0 * ALPHA, acc[ai][bj][m][1] * sc + r1 * ALPHA);
;             } }
;     }
	v_mov_b32_e32 v8, v184
	v_mov_b32_e32 v9, v185
	v_mov_b32_e32 v10, v186
	v_mov_b32_e32 v11, v187
	v_mov_b32_e32 v12, v188
	v_mov_b32_e32 v13, v189
	v_mov_b32_e32 v14, v190
	v_mov_b32_e32 v15, v191
	v_lshlrev_b64 v[16:17], 1, v[4:5]
	v_lshl_add_u64 v[20:21], s[6:7], 0, v[16:17]
	v_lshlrev_b32_e32 v4, 16, v8
	v_and_b32_e32 v5, 0xffff0000, v8
	v_lshlrev_b32_e32 v6, 16, v9
	v_and_b32_e32 v7, 0xffff0000, v9
	v_lshlrev_b32_e32 v8, 16, v10
	v_and_b32_e32 v9, 0xffff0000, v10
	v_lshlrev_b32_e32 v10, 16, v11
	v_and_b32_e32 v11, 0xffff0000, v11
	v_lshlrev_b32_e32 v22, 16, v12
	v_and_b32_e32 v23, 0xffff0000, v12
	v_lshlrev_b32_e32 v12, 16, v13
	v_and_b32_e32 v13, 0xffff0000, v13
	v_lshlrev_b32_e32 v24, 16, v14
	v_and_b32_e32 v25, 0xffff0000, v14
	v_lshlrev_b32_e32 v14, 16, v15
	v_and_b32_e32 v15, 0xffff0000, v15
	v_pk_mul_f32 v[4:5], v[4:5], s[12:13] op_sel_hi:[1,0]
	v_pk_mul_f32 v[6:7], v[6:7], s[12:13] op_sel_hi:[1,0]
	v_pk_mul_f32 v[8:9], v[8:9], s[12:13] op_sel_hi:[1,0]
	v_pk_mul_f32 v[10:11], v[10:11], s[12:13] op_sel_hi:[1,0]
	v_pk_mul_f32 v[22:23], v[22:23], s[12:13] op_sel_hi:[1,0]
	v_pk_mul_f32 v[12:13], v[12:13], s[12:13] op_sel_hi:[1,0]
	v_pk_mul_f32 v[24:25], v[24:25], s[12:13] op_sel_hi:[1,0]
	v_pk_mul_f32 v[14:15], v[14:15], s[12:13] op_sel_hi:[1,0]
	v_pk_fma_f32 v[6:7], v[128:129], s[14:15], v[6:7] op_sel_hi:[1,0,1]
	v_pk_fma_f32 v[4:5], v[126:127], s[14:15], v[4:5] op_sel_hi:[1,0,1]
	v_pk_fma_f32 v[10:11], v[124:125], s[14:15], v[10:11] op_sel_hi:[1,0,1]
	v_pk_fma_f32 v[8:9], v[122:123], s[14:15], v[8:9] op_sel_hi:[1,0,1]
	v_pk_fma_f32 v[12:13], v[120:121], s[14:15], v[12:13] op_sel_hi:[1,0,1]
	v_pk_fma_f32 v[22:23], v[118:119], s[14:15], v[22:23] op_sel_hi:[1,0,1]
	v_pk_fma_f32 v[14:15], v[116:117], s[14:15], v[14:15] op_sel_hi:[1,0,1]
	v_pk_fma_f32 v[24:25], v[114:115], s[14:15], v[24:25] op_sel_hi:[1,0,1]
	v_cvt_pk_bf16_f32 v4, v4, v5
	v_cvt_pk_bf16_f32 v5, v6, v7
	v_cvt_pk_bf16_f32 v6, v8, v9
	v_cvt_pk_bf16_f32 v7, v10, v11
	v_cvt_pk_bf16_f32 v8, v22, v23
	v_cvt_pk_bf16_f32 v9, v12, v13
	v_cvt_pk_bf16_f32 v10, v24, v25
	v_cvt_pk_bf16_f32 v11, v14, v15
	global_store_dwordx4 v[18:19], v[4:7], off
	global_store_dwordx4 v[18:19], v[8:11], off offset:256
	s_nop 1
	s_waitcnt vmcnt(14)
	v_mov_b32_e32 v4, v192
	v_mov_b32_e32 v5, v193
	v_mov_b32_e32 v6, v194
	v_mov_b32_e32 v7, v195
	v_mov_b32_e32 v8, v196
	v_mov_b32_e32 v9, v197
	v_mov_b32_e32 v10, v198
	v_mov_b32_e32 v11, v199
	v_lshl_add_u64 v[12:13], v[2:3], 0, s[16:17]
	v_lshl_add_u64 v[14:15], s[8:9], 0, v[16:17]
	v_lshl_add_u64 v[16:17], s[6:7], 0, v[12:13]
	v_lshl_add_u64 v[12:13], s[8:9], 0, v[12:13]
	v_lshlrev_b32_e32 v18, 16, v4
	v_and_b32_e32 v19, 0xffff0000, v4
	v_lshlrev_b32_e32 v4, 16, v5
	v_and_b32_e32 v5, 0xffff0000, v5
	v_lshlrev_b32_e32 v20, 16, v6
	v_and_b32_e32 v21, 0xffff0000, v6
	v_lshlrev_b32_e32 v6, 16, v7
	v_and_b32_e32 v7, 0xffff0000, v7
	v_lshlrev_b32_e32 v22, 16, v8
	v_and_b32_e32 v23, 0xffff0000, v8
	v_lshlrev_b32_e32 v8, 16, v9
	v_and_b32_e32 v9, 0xffff0000, v9
	v_lshlrev_b32_e32 v24, 16, v10
	v_and_b32_e32 v25, 0xffff0000, v10
	v_lshlrev_b32_e32 v10, 16, v11
	v_and_b32_e32 v11, 0xffff0000, v11
	v_pk_mul_f32 v[18:19], v[18:19], s[12:13] op_sel_hi:[1,0]
	v_pk_mul_f32 v[4:5], v[4:5], s[12:13] op_sel_hi:[1,0]
	v_pk_mul_f32 v[20:21], v[20:21], s[12:13] op_sel_hi:[1,0]
	v_pk_mul_f32 v[6:7], v[6:7], s[12:13] op_sel_hi:[1,0]
	v_pk_mul_f32 v[22:23], v[22:23], s[12:13] op_sel_hi:[1,0]
	v_pk_mul_f32 v[8:9], v[8:9], s[12:13] op_sel_hi:[1,0]
	v_pk_mul_f32 v[24:25], v[24:25], s[12:13] op_sel_hi:[1,0]
	v_pk_mul_f32 v[10:11], v[10:11], s[12:13] op_sel_hi:[1,0]
	v_pk_fma_f32 v[26:27], v[112:113], s[14:15], v[4:5] op_sel_hi:[1,0,1]
	v_pk_fma_f32 v[4:5], v[110:111], s[14:15], v[18:19] op_sel_hi:[1,0,1]
	v_pk_fma_f32 v[18:19], v[108:109], s[14:15], v[6:7] op_sel_hi:[1,0,1]
	v_pk_fma_f32 v[6:7], v[106:107], s[14:15], v[20:21] op_sel_hi:[1,0,1]
	v_pk_fma_f32 v[20:21], v[104:105], s[14:15], v[8:9] op_sel_hi:[1,0,1]
	v_pk_fma_f32 v[8:9], v[102:103], s[14:15], v[22:23] op_sel_hi:[1,0,1]
	v_pk_fma_f32 v[22:23], v[100:101], s[14:15], v[10:11] op_sel_hi:[1,0,1]
	v_pk_fma_f32 v[10:11], v[98:99], s[14:15], v[24:25] op_sel_hi:[1,0,1]
	v_cvt_pk_bf16_f32 v4, v4, v5
	v_cvt_pk_bf16_f32 v5, v26, v27
	v_cvt_pk_bf16_f32 v6, v6, v7
	v_cvt_pk_bf16_f32 v7, v18, v19
	v_cvt_pk_bf16_f32 v8, v8, v9
	v_cvt_pk_bf16_f32 v9, v20, v21
	v_cvt_pk_bf16_f32 v10, v10, v11
	v_cvt_pk_bf16_f32 v11, v22, v23
	global_store_dwordx4 v[14:15], v[4:7], off
	global_store_dwordx4 v[14:15], v[8:11], off offset:256
	s_nop 1
	s_waitcnt vmcnt(14)
; __device__ __forceinline__ u32x4 pack8(const f32x4 v0, const f32x4 v1) { u32x4 w; w.x = cvt_pk_bf16(v0[0], v0[1]); w.y = cvt_pk_bf16(v0[2], v0[3]); w.z = cvt_pk_bf16(v1[0], v1[1]); w.w = cvt_pk_bf16(v1[2], v1[3]); return w; }
; #define EPI_ROWLOOP for (int ai = 0; ai < 2; ++ai) _Pragma("unroll") for (int m = 0; m < 4; ++m)
;     __device__ __forceinline__ void operator()(const f32x4 (&acc)[2][2][4][2], const pg8::Unit& u, int wr, int wc, int fr, int fq) const {
;         const int row0 = u.pm * 256 + wr * 64 + fr, c0 = u.pn * 256 + wc * 32 + 8 * fq;
; #pragma unroll
;         EPI_ROWLOOP { const size_t ro = (size_t)(row0 + ai * 128 + m * 16) * 1024 + c0;
; #pragma unroll
;             for (int bj = 0; bj < 2; ++bj) {
;                 f32x4 r0, r1;
;                 if (resf) { r0 = *(const f32x4*)(resf + ro + bj * 128); r1 = *(const f32x4*)(resf + ro + bj * 128 + 4); }
;                 else { const u32x4 xv = *(const u32x4*)(resb + ro + bj * 128);
;                     r0[0] = __uint_as_float(xv.x << 16); r0[1] = __uint_as_float(xv.x & 0xffff0000u); r0[2] = __uint_as_float(xv.y << 16); r0[3] = __uint_as_float(xv.y & 0xffff0000u);
;                     r1[0] = __uint_as_float(xv.z << 16); r1[1] = __uint_as_float(xv.z & 0xffff0000u); r1[2] = __uint_as_float(xv.w << 16); r1[3] = __uint_as_float(xv.w & 0xffff0000u); }
;                 *(u32x4*)(Y + ro + bj * 128) = pack8(acc[ai][bj][m][0] * sc + r0 * ALPHA, acc[ai][bj][m][1] * sc + r1 * ALPHA);
;             } }
;     }
	v_mov_b32_e32 v4, v200
	v_mov_b32_e32 v5, v201
	v_mov_b32_e32 v6, v202
	v_mov_b32_e32 v7, v203
	v_mov_b32_e32 v8, v204
	v_mov_b32_e32 v9, v205
	v_mov_b32_e32 v10, v206
	v_mov_b32_e32 v11, v207
	v_lshl_add_u64 v[14:15], v[2:3], 0, s[18:19]
	v_lshl_add_u64 v[16:17], s[6:7], 0, v[14:15]
	v_lshl_add_u64 v[14:15], s[8:9], 0, v[14:15]
	v_lshlrev_b32_e32 v18, 16, v4
	v_and_b32_e32 v19, 0xffff0000, v4
	v_lshlrev_b32_e32 v4, 16, v5
	v_and_b32_e32 v5, 0xffff0000, v5
	v_lshlrev_b32_e32 v20, 16, v6
	v_and_b32_e32 v21, 0xffff0000, v6
	v_lshlrev_b32_e32 v6, 16, v7
	v_and_b32_e32 v7, 0xffff0000, v7
	v_lshlrev_b32_e32 v22, 16, v8
	v_and_b32_e32 v23, 0xffff0000, v8
	v_lshlrev_b32_e32 v8, 16, v9
	v_and_b32_e32 v9, 0xffff0000, v9
	v_lshlrev_b32_e32 v24, 16, v10
	v_and_b32_e32 v25, 0xffff0000, v10
	v_lshlrev_b32_e32 v10, 16, v11
	v_and_b32_e32 v11, 0xffff0000, v11
	v_pk_mul_f32 v[18:19], v[18:19], s[12:13] op_sel_hi:[1,0]
	v_pk_mul_f32 v[4:5], v[4:5], s[12:13] op_sel_hi:[1,0]
	v_pk_mul_f32 v[20:21], v[20:21], s[12:13] op_sel_hi:[1,0]
	v_pk_mul_f32 v[6:7], v[6:7], s[12:13] op_sel_hi:[1,0]
	v_pk_mul_f32 v[22:23], v[22:23], s[12:13] op_sel_hi:[1,0]
	v_pk_mul_f32 v[8:9], v[8:9], s[12:13] op_sel_hi:[1,0]
	v_pk_mul_f32 v[24:25], v[24:25], s[12:13] op_sel_hi:[1,0]
	v_pk_mul_f32 v[10:11], v[10:11], s[12:13] op_sel_hi:[1,0]
	v_pk_fma_f32 v[26:27], v[96:97], s[14:15], v[4:5] op_sel_hi:[1,0,1]
	v_pk_fma_f32 v[4:5], v[94:95], s[14:15], v[18:19] op_sel_hi:[1,0,1]
	v_pk_fma_f32 v[18:19], v[92:93], s[14:15], v[6:7] op_sel_hi:[1,0,1]
	v_pk_fma_f32 v[6:7], v[90:91], s[14:15], v[20:21] op_sel_hi:[1,0,1]
	v_pk_fma_f32 v[20:21], v[88:89], s[14:15], v[8:9] op_sel_hi:[1,0,1]
	v_pk_fma_f32 v[8:9], v[86:87], s[14:15], v[22:23] op_sel_hi:[1,0,1]
	v_pk_fma_f32 v[22:23], v[84:85], s[14:15], v[10:11] op_sel_hi:[1,0,1]
	v_pk_fma_f32 v[10:11], v[82:83], s[14:15], v[24:25] op_sel_hi:[1,0,1]
	v_cvt_pk_bf16_f32 v4, v4, v5
	v_cvt_pk_bf16_f32 v5, v26, v27
	v_cvt_pk_bf16_f32 v6, v6, v7
	v_cvt_pk_bf16_f32 v7, v18, v19
	v_cvt_pk_bf16_f32 v8, v8, v9
	v_cvt_pk_bf16_f32 v9, v20, v21
	v_cvt_pk_bf16_f32 v10, v10, v11
	v_cvt_pk_bf16_f32 v11, v22, v23
	global_store_dwordx4 v[12:13], v[4:7], off
	global_store_dwordx4 v[12:13], v[8:11], off offset:256
	s_nop 1
	s_waitcnt vmcnt(14)
	v_mov_b32_e32 v4, v224
	v_mov_b32_e32 v5, v225
	v_mov_b32_e32 v6, v226
	v_mov_b32_e32 v7, v227
	v_mov_b32_e32 v8, v228
	v_mov_b32_e32 v9, v229
	v_mov_b32_e32 v10, v230
	v_mov_b32_e32 v11, v231
	v_lshl_add_u64 v[12:13], v[2:3], 0, s[20:21]
	v_lshl_add_u64 v[16:17], s[6:7], 0, v[12:13]
	v_lshl_add_u64 v[12:13], s[8:9], 0, v[12:13]
	v_lshlrev_b32_e32 v18, 16, v4
	v_and_b32_e32 v19, 0xffff0000, v4
	v_lshlrev_b32_e32 v4, 16, v5
	v_and_b32_e32 v5, 0xffff0000, v5
	v_lshlrev_b32_e32 v20, 16, v6
	v_and_b32_e32 v21, 0xffff0000, v6
	v_lshlrev_b32_e32 v6, 16, v7
	v_and_b32_e32 v7, 0xffff0000, v7
	v_lshlrev_b32_e32 v22, 16, v8
	v_and_b32_e32 v23, 0xffff0000, v8
	v_lshlrev_b32_e32 v8, 16, v9
	v_and_b32_e32 v9, 0xffff0000, v9
	v_lshlrev_b32_e32 v24, 16, v10
	v_and_b32_e32 v25, 0xffff0000, v10
	v_lshlrev_b32_e32 v10, 16, v11
	v_and_b32_e32 v11, 0xffff0000, v11
	v_pk_mul_f32 v[18:19], v[18:19], s[12:13] op_sel_hi:[1,0]
	v_pk_mul_f32 v[4:5], v[4:5], s[12:13] op_sel_hi:[1,0]
	v_pk_mul_f32 v[20:21], v[20:21], s[12:13] op_sel_hi:[1,0]
	v_pk_mul_f32 v[6:7], v[6:7], s[12:13] op_sel_hi:[1,0]
	v_pk_mul_f32 v[22:23], v[22:23], s[12:13] op_sel_hi:[1,0]
	v_pk_mul_f32 v[8:9], v[8:9], s[12:13] op_sel_hi:[1,0]
	v_pk_mul_f32 v[24:25], v[24:25], s[12:13] op_sel_hi:[1,0]
	v_pk_mul_f32 v[10:11], v[10:11], s[12:13] op_sel_hi:[1,0]
	v_pk_fma_f32 v[26:27], v[80:81], s[14:15], v[4:5] op_sel_hi:[1,0,1]
	v_pk_fma_f32 v[4:5], v[78:79], s[14:15], v[18:19] op_sel_hi:[1,0,1]
	v_pk_fma_f32 v[18:19], v[76:77], s[14:15], v[6:7] op_sel_hi:[1,0,1]
	v_pk_fma_f32 v[6:7], v[74:75], s[14:15], v[20:21] op_sel_hi:[1,0,1]
	v_pk_fma_f32 v[20:21], v[72:73], s[14:15], v[8:9] op_sel_hi:[1,0,1]
	v_pk_fma_f32 v[8:9], v[70:71], s[14:15], v[22:23] op_sel_hi:[1,0,1]
	v_pk_fma_f32 v[22:23], v[68:69], s[14:15], v[10:11] op_sel_hi:[1,0,1]
	v_pk_fma_f32 v[10:11], v[66:67], s[14:15], v[24:25] op_sel_hi:[1,0,1]
	v_cvt_pk_bf16_f32 v4, v4, v5
	v_cvt_pk_bf16_f32 v5, v26, v27
	v_cvt_pk_bf16_f32 v6, v6, v7
	v_cvt_pk_bf16_f32 v7, v18, v19
	v_cvt_pk_bf16_f32 v8, v8, v9
	v_cvt_pk_bf16_f32 v9, v20, v21
	v_cvt_pk_bf16_f32 v10, v10, v11
	v_cvt_pk_bf16_f32 v11, v22, v23
	global_store_dwordx4 v[14:15], v[4:7], off
	global_store_dwordx4 v[14:15], v[8:11], off offset:256
	s_nop 1
	s_waitcnt vmcnt(14)
; __device__ __forceinline__ u32x4 pack8(const f32x4 v0, const f32x4 v1) { u32x4 w; w.x = cvt_pk_bf16(v0[0], v0[1]); w.y = cvt_pk_bf16(v0[2], v0[3]); w.z = cvt_pk_bf16(v1[0], v1[1]); w.w = cvt_pk_bf16(v1[2], v1[3]); return w; }
; #define EPI_ROWLOOP for (int ai = 0; ai < 2; ++ai) _Pragma("unroll") for (int m = 0; m < 4; ++m)
;     __device__ __forceinline__ void operator()(const f32x4 (&acc)[2][2][4][2], const pg8::Unit& u, int wr, int wc, int fr, int fq) const {
;         const int row0 = u.pm * 256 + wr * 64 + fr, c0 = u.pn * 256 + wc * 32 + 8 * fq;
; #pragma unroll
;         EPI_ROWLOOP { const size_t ro = (size_t)(row0 + ai * 128 + m * 16) * 1024 + c0;
; #pragma unroll
;             for (int bj = 0; bj < 2; ++bj) {
;                 f32x4 r0, r1;
;                 if (resf) { r0 = *(const f32x4*)(resf + ro + bj * 128); r1 = *(const f32x4*)(resf + ro + bj * 128 + 4); }
;                 else { const u32x4 xv = *(const u32x4*)(resb + ro + bj * 128);
;                     r0[0] = __uint_as_float(xv.x << 16); r0[1] = __uint_as_float(xv.x & 0xffff0000u); r0[2] = __uint_as_float(xv.y << 16); r0[3] = __uint_as_float(xv.y & 0xffff0000u);
;                     r1[0] = __uint_as_float(xv.z << 16); r1[1] = __uint_as_float(xv.z & 0xffff0000u); r1[2] = __uint_as_float(xv.w << 16); r1[3] = __uint_as_float(xv.w & 0xffff0000u); }
;                 *(u32x4*)(Y + ro + bj * 128) = pack8(acc[ai][bj][m][0] * sc + r0 * ALPHA, acc[ai][bj][m][1] * sc + r1 * ALPHA);
;             } }
;     }
	v_mov_b32_e32 v4, v232
	v_mov_b32_e32 v5, v233
	v_mov_b32_e32 v6, v234
	v_mov_b32_e32 v7, v235
	v_mov_b32_e32 v8, v236
	v_mov_b32_e32 v9, v237
	v_mov_b32_e32 v10, v238
	v_mov_b32_e32 v11, v239
	v_lshl_add_u64 v[14:15], v[2:3], 0, s[22:23]
	v_lshl_add_u64 v[16:17], s[6:7], 0, v[14:15]
	v_lshlrev_b32_e32 v2, 16, v4
	v_and_b32_e32 v3, 0xffff0000, v4
	v_lshlrev_b32_e32 v4, 16, v5
	v_and_b32_e32 v5, 0xffff0000, v5
	v_lshlrev_b32_e32 v18, 16, v6
	v_and_b32_e32 v19, 0xffff0000, v6
	v_lshlrev_b32_e32 v6, 16, v7
	v_and_b32_e32 v7, 0xffff0000, v7
	v_lshlrev_b32_e32 v20, 16, v8
	v_and_b32_e32 v21, 0xffff0000, v8
	v_lshlrev_b32_e32 v8, 16, v9
	v_and_b32_e32 v9, 0xffff0000, v9
	v_lshlrev_b32_e32 v22, 16, v10
	v_and_b32_e32 v23, 0xffff0000, v10
	v_lshlrev_b32_e32 v10, 16, v11
	v_and_b32_e32 v11, 0xffff0000, v11
	v_pk_mul_f32 v[2:3], v[2:3], s[12:13] op_sel_hi:[1,0]
	v_pk_mul_f32 v[4:5], v[4:5], s[12:13] op_sel_hi:[1,0]
	v_pk_mul_f32 v[18:19], v[18:19], s[12:13] op_sel_hi:[1,0]
	v_pk_mul_f32 v[6:7], v[6:7], s[12:13] op_sel_hi:[1,0]
	v_pk_mul_f32 v[20:21], v[20:21], s[12:13] op_sel_hi:[1,0]
	v_pk_mul_f32 v[8:9], v[8:9], s[12:13] op_sel_hi:[1,0]
	v_pk_mul_f32 v[22:23], v[22:23], s[12:13] op_sel_hi:[1,0]
	v_pk_mul_f32 v[10:11], v[10:11], s[12:13] op_sel_hi:[1,0]
	v_pk_fma_f32 v[4:5], v[64:65], s[14:15], v[4:5] op_sel_hi:[1,0,1]
	v_pk_fma_f32 v[2:3], v[62:63], s[14:15], v[2:3] op_sel_hi:[1,0,1]
	v_pk_fma_f32 v[6:7], v[60:61], s[14:15], v[6:7] op_sel_hi:[1,0,1]
	v_pk_fma_f32 v[18:19], v[58:59], s[14:15], v[18:19] op_sel_hi:[1,0,1]
	v_pk_fma_f32 v[8:9], v[52:53], s[14:15], v[8:9] op_sel_hi:[1,0,1]
	v_pk_fma_f32 v[20:21], v[50:51], s[14:15], v[20:21] op_sel_hi:[1,0,1]
	v_pk_fma_f32 v[10:11], v[56:57], s[14:15], v[10:11] op_sel_hi:[1,0,1]
	v_pk_fma_f32 v[22:23], v[54:55], s[14:15], v[22:23] op_sel_hi:[1,0,1]
	v_cvt_pk_bf16_f32 v2, v2, v3
	v_cvt_pk_bf16_f32 v3, v4, v5
	v_cvt_pk_bf16_f32 v4, v18, v19
	v_cvt_pk_bf16_f32 v5, v6, v7
	v_cvt_pk_bf16_f32 v6, v20, v21
	v_cvt_pk_bf16_f32 v7, v8, v9
	v_cvt_pk_bf16_f32 v8, v22, v23
	v_cvt_pk_bf16_f32 v9, v10, v11
	global_store_dwordx4 v[12:13], v[2:5], off
	global_store_dwordx4 v[12:13], v[6:9], off offset:256
	s_nop 1
	s_waitcnt vmcnt(14)
	v_mov_b32_e32 v2, v240
	v_mov_b32_e32 v3, v241
	v_mov_b32_e32 v4, v242
	v_mov_b32_e32 v5, v243
	v_mov_b32_e32 v6, v244
	v_mov_b32_e32 v7, v245
	v_mov_b32_e32 v8, v246
	v_mov_b32_e32 v9, v247
	v_lshl_add_u64 v[10:11], s[8:9], 0, v[14:15]
	v_lshlrev_b32_e32 v12, 16, v2
	v_and_b32_e32 v13, 0xffff0000, v2
	v_lshlrev_b32_e32 v2, 16, v3
	v_and_b32_e32 v3, 0xffff0000, v3
	v_lshlrev_b32_e32 v14, 16, v4
	v_and_b32_e32 v15, 0xffff0000, v4
	v_lshlrev_b32_e32 v4, 16, v5
	v_and_b32_e32 v5, 0xffff0000, v5
	v_lshlrev_b32_e32 v16, 16, v6
	v_and_b32_e32 v17, 0xffff0000, v6
	v_lshlrev_b32_e32 v6, 16, v7
	v_and_b32_e32 v7, 0xffff0000, v7
	v_lshlrev_b32_e32 v18, 16, v8
	v_and_b32_e32 v19, 0xffff0000, v8
	v_lshlrev_b32_e32 v8, 16, v9
	v_and_b32_e32 v9, 0xffff0000, v9
	v_pk_mul_f32 v[12:13], v[12:13], s[12:13] op_sel_hi:[1,0]
	v_pk_mul_f32 v[2:3], v[2:3], s[12:13] op_sel_hi:[1,0]
	v_pk_mul_f32 v[14:15], v[14:15], s[12:13] op_sel_hi:[1,0]
	v_pk_mul_f32 v[4:5], v[4:5], s[12:13] op_sel_hi:[1,0]
	v_pk_mul_f32 v[16:17], v[16:17], s[12:13] op_sel_hi:[1,0]
	v_pk_mul_f32 v[6:7], v[6:7], s[12:13] op_sel_hi:[1,0]
	v_pk_mul_f32 v[18:19], v[18:19], s[12:13] op_sel_hi:[1,0]
	v_pk_mul_f32 v[8:9], v[8:9], s[12:13] op_sel_hi:[1,0]
	v_pk_fma_f32 v[20:21], v[48:49], s[14:15], v[2:3] op_sel_hi:[1,0,1]
	v_pk_fma_f32 v[2:3], v[46:47], s[14:15], v[12:13] op_sel_hi:[1,0,1]
	v_pk_fma_f32 v[12:13], v[44:45], s[14:15], v[4:5] op_sel_hi:[1,0,1]
	v_pk_fma_f32 v[4:5], v[42:43], s[14:15], v[14:15] op_sel_hi:[1,0,1]
	v_pk_fma_f32 v[14:15], v[40:41], s[14:15], v[6:7] op_sel_hi:[1,0,1]
	v_pk_fma_f32 v[6:7], v[38:39], s[14:15], v[16:17] op_sel_hi:[1,0,1]
	v_pk_fma_f32 v[16:17], v[36:37], s[14:15], v[8:9] op_sel_hi:[1,0,1]
	v_pk_fma_f32 v[8:9], v[34:35], s[14:15], v[18:19] op_sel_hi:[1,0,1]
	v_cvt_pk_bf16_f32 v2, v2, v3
	v_cvt_pk_bf16_f32 v3, v20, v21
	v_cvt_pk_bf16_f32 v4, v4, v5
	v_cvt_pk_bf16_f32 v5, v12, v13
	v_cvt_pk_bf16_f32 v6, v6, v7
	v_cvt_pk_bf16_f32 v7, v14, v15
	v_cvt_pk_bf16_f32 v8, v8, v9
	v_cvt_pk_bf16_f32 v9, v16, v17
	global_store_dwordx4 v[10:11], v[2:5], off
	global_store_dwordx4 v[10:11], v[6:9], off offset:256
	s_cbranch_vccnz .LBB0_2352
	s_andn2_b64 vcc, exec, s[2:3]
	s_cbranch_vccnz .LBB0_2351
	s_barrier
	s_branch .LBB0_2351
